# phase-entry parameter reloads from LDS: all reads of a chain issued up front into distinct registers, one wait (20 chains, 109 reads)
# baseline (speedup 1.0000x reference)
.LBB0_6:
	s_or_b64 exec, exec, s[4:5]
	s_lshr_b32 s33, s0, 6
	s_mov_b32 s0, 0
	s_mov_b32 s1, s33
	v_mbcnt_lo_u32_b32 v0, -1, s0
	v_mbcnt_hi_u32_b32 v0, -1, v0
	v_readlane_b32 s6, v254, 0
	v_lshl_or_b32 v0, s1, 6, v0
	s_mov_b32 s0, 0
	s_add_i32 s0, s0, 0x20010
	v_mov_b32_e32 v1, s0
	s_mov_b32 s0, 0
	v_mov_b32_e32 v251, 0x20000
	ds_read_b64 v[206:207], v251 offset:16
	ds_read_b64 v[208:209], v251 offset:40
	ds_read_b64 v[210:211], v251 offset:288
	ds_read_b64 v[212:213], v251 offset:288
	ds_read_b64 v[214:215], v251 offset:288
	s_add_i32 s0, s0, 0x20028
	v_mov_b32_e32 v1, s0
	s_mov_b32 s1, 0
	s_add_i32 s1, s1, 0x20120
	v_mov_b32_e32 v1, s1
	s_mov_b32 s1, 0
	s_waitcnt lgkmcnt(1)
	v_readfirstlane_b32 s5, v207
	v_readfirstlane_b32 s4, v206
	s_add_i32 s1, s1, 0x20120
	s_mov_b32 s0, 0
	v_mov_b32_e32 v1, s1
	s_waitcnt lgkmcnt(1)
	v_readfirstlane_b32 s11, v209
	v_readfirstlane_b32 s10, v208
	s_add_i32 s0, s0, 0x20120
	v_mov_b32_e32 v1, s0
	v_ashrrev_i32_e32 v16, 6, v0
	s_lshl_b32 s12, s6, 3
	v_readlane_b32 s7, v254, 1
	v_add_u32_e32 v17, s12, v16
	s_movk_i32 s8, 0x2000
	s_waitcnt lgkmcnt(2)
	v_readfirstlane_b32 s3, v211
	v_readfirstlane_b32 s13, v210
	s_waitcnt lgkmcnt(1)
	v_readfirstlane_b32 s1, v213
	v_readfirstlane_b32 s7, v212
	s_waitcnt lgkmcnt(0)
	v_readfirstlane_b32 s0, v215
	v_readfirstlane_b32 s2, v214
	v_cmp_gt_i32_e32 vcc, s8, v17
	v_and_b32_e32 v2, 63, v0
	s_and_saveexec_b64 s[8:9], vcc
	s_cbranch_execz .LBB0_11
	s_add_u32 s14, s13, 0x3600
	s_addc_u32 s15, s3, 0
	s_add_u32 s16, s7, 0x5734fd00
	s_addc_u32 s17, s1, 0
	s_add_u32 s2, s2, 0x57327d00
	s_addc_u32 s3, s0, 0
	v_add_u32_e32 v28, 0xfffff800, v17
	v_ashrrev_i32_e32 v17, 31, v16
	s_ashr_i32 s13, s12, 31
	v_lshlrev_b32_e32 v18, 2, v2
	v_lshl_add_u64 v[20:21], v[16:17], 0, s[12:13]
	v_lshlrev_b32_e32 v4, 4, v2
	v_mov_b32_e32 v5, 0
	v_xor_b32_e32 v1, 0x80, v18
	v_xor_b32_e32 v3, 64, v18
	v_xor_b32_e32 v24, 32, v18
	v_xor_b32_e32 v25, 16, v18
	v_xor_b32_e32 v26, 8, v18
	v_xor_b32_e32 v27, 4, v18
	v_lshlrev_b64 v[18:19], 12, v[20:21]
	v_or_b32_e32 v8, 0x1000, v4
	v_mov_b32_e32 v9, v5
	v_or_b32_e32 v10, 0x1400, v4
	v_mov_b32_e32 v11, v5
	v_or_b32_e32 v12, 0x1800, v4
	v_mov_b32_e32 v13, v5
	v_or_b32_e32 v14, 0x1c00, v4
	v_mov_b32_e32 v15, v5
	v_lshl_or_b32 v18, v2, 3, v18
	v_lshlrev_b64 v[22:23], 13, v[20:21]
	v_cmp_eq_u32_e32 vcc, 0, v2
	v_lshl_add_u64 v[6:7], s[10:11], 0, v[4:5]
	s_movk_i32 s0, 0x1000
	v_lshl_add_u64 v[8:9], s[10:11], 0, v[8:9]
	v_lshl_add_u64 v[10:11], s[10:11], 0, v[10:11]
	v_lshl_add_u64 v[12:13], s[10:11], 0, v[12:13]
	v_lshl_add_u64 v[14:15], s[10:11], 0, v[14:15]
	v_lshl_add_u64 v[16:17], v[20:21], 2, s[2:3]
	v_lshl_add_u64 v[18:19], s[16:17], 0, v[18:19]
	v_lshl_add_u64 v[20:21], s[4:5], 0, v[22:23]
	v_lshl_add_u64 v[22:23], s[14:15], 0, v[22:23]
	s_mov_b64 s[10:11], 0
	s_mov_b64 s[12:13], 0x2000
	s_mov_b64 s[14:15], 0x800000
	s_mov_b64 s[16:17], 0x1000000
	s_movk_i32 s1, 0x17ff
	s_branch .LBB0_9

.LBB0_20:
	s_or_b64 exec, exec, s[4:5]
	s_mov_b32 s0, 0
	s_mov_b32 s1, s33
	v_mbcnt_lo_u32_b32 v0, -1, s0
	v_mbcnt_hi_u32_b32 v0, -1, v0
	v_lshl_or_b32 v0, s1, 6, v0
	v_readlane_b32 s0, v254, 0
	v_readlane_b32 s1, v254, 1
	s_mov_b32 s1, 0
	s_add_i32 s1, s1, 0x20020
	v_mov_b32_e32 v1, s1
	s_mov_b32 s1, 0
	v_mov_b32_e32 v251, 0x20000
	ds_read_b64 v[206:207], v251 offset:32
	ds_read_b64 v[208:209], v251 offset:288
	ds_read_b64 v[210:211], v251 offset:288
	ds_read_b64 v[212:213], v251 offset:288
	ds_read_b64 v[214:215], v251 offset:288
	s_add_i32 s1, s1, 0x20120
	v_mov_b32_e32 v1, s1
	s_mov_b32 s4, 0
	s_add_i32 s4, s4, 0x20120
	v_mov_b32_e32 v1, s4
	s_mov_b32 s4, 0
	s_waitcnt lgkmcnt(0)
	v_readfirstlane_b32 s11, v207
	v_readfirstlane_b32 s10, v206
	s_add_i32 s4, s4, 0x20120
	s_mov_b32 s1, 0
	v_mov_b32_e32 v1, s4
	v_readfirstlane_b32 s2, v209
	v_readfirstlane_b32 s3, v208
	s_add_i32 s1, s1, 0x20120
	v_mov_b32_e32 v1, s1
	s_ashr_i32 s1, s0, 31
	s_lshl_b64 s[0:1], s[0:1], 9
	v_ashrrev_i32_e32 v1, 31, v0
	v_lshl_add_u64 v[0:1], s[0:1], 0, v[0:1]
	s_mov_b64 s[0:1], 0x30000
	s_waitcnt lgkmcnt(0)
	v_readfirstlane_b32 s7, v211
	v_readfirstlane_b32 s9, v210
	v_readfirstlane_b32 s5, v213
	v_readfirstlane_b32 s8, v212
	v_readfirstlane_b32 s4, v215
	v_readfirstlane_b32 s6, v214
	v_cmp_gt_i64_e32 vcc, s[0:1], v[0:1]
	s_and_saveexec_b64 s[0:1], vcc
	s_cbranch_execz .LBB0_27
	s_add_u32 s14, s3, 0x1a5cb600
	s_addc_u32 s15, s2, 0
	s_add_u32 s16, s9, 0x1a60b600
	s_addc_u32 s17, s7, 0
	s_add_u32 s18, s8, 0x1a64b600
	s_addc_u32 s19, s5, 0
	s_add_u32 s20, s6, 0x1a6cb600
	s_mov_b32 s24, 0x69a05c01
	s_mov_b32 s26, 0x652b82fe
	s_mov_b32 s28, 0xfefa39ef
	s_mov_b32 s30, 0x3b39803f
	s_mov_b32 s34, 0x6a5dcb37
	s_mov_b32 s36, 0x6dc9c883
	s_mov_b32 s38, 0x54442d18
	s_mov_b32 s40, 0x33145c07
	s_mov_b32 s42, 0
	s_mov_b32 s44, 0
	s_mov_b32 s46, 0
	s_mov_b32 s48, 0
	s_mov_b32 s50, 0
	s_mov_b32 s52, 0
	s_mov_b32 s54, 0
	s_mov_b32 s56, 0
	s_mov_b32 s58, 0
	s_mov_b32 s60, 0
	s_mov_b32 s62, 0
	s_mov_b32 s64, 0
	s_mov_b32 s66, 0
	s_mov_b32 s68, 0
	s_mov_b32 s70, 0
	s_mov_b32 s72, 0
	s_mov_b32 s74, 0
	s_mov_b32 s76, 0
	s_mov_b32 s78, 0
	s_mov_b32 s80, 0
	s_mov_b32 s82, 0
	s_mov_b32 s84, 0
	s_mov_b32 s86, 0
	s_mov_b32 s88, 0
	s_mov_b32 s90, 0
	s_mov_b32 s92, 0
	s_mov_b32 s94, 0
	s_addc_u32 s21, s4, 0
	s_mov_b64 s[22:23], 0
	s_mov_b32 s3, 0xaaaaaaab
	v_mov_b32_e32 v3, 0
	s_mov_b32 s12, 0x2aaaaaaa
	s_movk_i32 s13, 0xffe8
	s_mov_b32 s25, 0x402a3ea6
	s_mov_b32 s27, 0x3ff71547
	s_mov_b32 s29, 0xbfe62e42
	s_mov_b32 s31, 0xbc7abc9e
	v_mov_b32_e32 v4, 0xfca7ab0c
	v_mov_b32_e32 v5, 0x3e928af3
	s_mov_b32 s35, 0x3e5ade15
	v_mov_b32_e32 v6, 0x623fde64
	v_mov_b32_e32 v7, 0x3ec71dee
	v_mov_b32_e32 v8, 0x7c89e6b0
	v_mov_b32_e32 v9, 0x3efa0199
	s_mov_b32 s37, 0x3fc45f30
	s_mov_b32 s39, 0xc01921fb
	s_mov_b32 s41, 0xbcb1a626
	s_mov_b32 s43, 0x40896000
	s_mov_b32 s45, 0x4087a000
	s_mov_b32 s47, 0x4085f000
	s_mov_b32 s49, 0x40845000
	s_mov_b32 s51, 0x4082c000
	s_mov_b32 s53, 0x40814000
	s_mov_b32 s55, 0x407fa000
	s_mov_b32 s57, 0x407ce000
	s_mov_b32 s59, 0x407a4000
	s_mov_b32 s61, 0x4077c000
	s_mov_b32 s63, 0x40756000
	s_mov_b32 s65, 0x40732000
	s_mov_b32 s67, 0x40710000
	s_mov_b32 s69, 0x406e0000
	s_mov_b32 s71, 0x406a4000
	s_mov_b32 s73, 0x4066c000
	s_mov_b32 s75, 0x40638000
	s_mov_b32 s77, 0x40608000
	s_mov_b32 s79, 0x405b8000
	s_mov_b32 s81, 0x40568000
	s_mov_b32 s83, 0x40520000
	s_mov_b32 s85, 0x404c0000
	s_mov_b32 s87, 0x40450000
	s_mov_b32 s89, 0x403e0000
	s_mov_b32 s91, 0x40340000
	s_mov_b32 s93, 0x40280000
	s_mov_b32 s95, 0x40180000
	s_mov_b64 s[96:97], 0xffff
	v_mov_b32_e32 v10, 0x14761f6e
	v_mov_b32_e32 v11, 0x3f2a01a0
	v_mov_b32_e32 v12, 0x1852b7b0
	v_mov_b32_e32 v13, 0x3f56c16c
	v_mov_b32_e32 v14, 0x11122322
	v_mov_b32_e32 v15, 0x3f811111
	v_mov_b32_e32 v16, 0x555502a1
	v_mov_b32_e32 v17, 0x3fa55555
	v_mov_b32_e32 v18, 0x55555511
	v_mov_b32_e32 v19, 0x3fc55555
	v_mov_b32_e32 v20, 11
	v_mov_b32_e32 v21, 0x3fe00000
	v_mov_b32_e32 v34, 0x7ff00000
	s_branch .LBB0_23

.LBB0_148:
	s_or_b64 exec, exec, s[0:1]
	s_mov_b32 s0, s37
	s_mov_b32 s1, s33
	v_mbcnt_lo_u32_b32 v0, -1, s0
	v_mbcnt_hi_u32_b32 v0, -1, v0
	v_lshl_or_b32 v8, s1, 6, v0
	v_readlane_b32 s0, v254, 0
	s_mov_b32 s30, s0
	s_mov_b32 s0, s37
	s_add_i32 s0, s0, 0x20120
	v_mov_b32_e32 v0, s0
	v_mov_b32_e32 v251, 0x20000
	ds_read_b64 v[206:207], v251 offset:288
	ds_read_b64 v[208:209], v251 offset:288
	ds_read_b64 v[210:211], v251 offset:288
	ds_read_b64 v[212:213], v251 offset:288
	s_mov_b32 s0, 0
	s_add_i32 s0, s0, 0x20120
	s_mov_b32 s15, s60
	s_waitcnt lgkmcnt(0)
	v_readfirstlane_b32 s14, v206
	v_mov_b32_e32 v0, s0
	s_mov_b32 s0, 0
	v_readfirstlane_b32 s2, v207
	s_add_i32 s0, s0, 0x20120
	v_mov_b32_e32 v2, s0
	s_mov_b32 s0, 0
	s_add_i32 s0, s0, 0x20120
	v_mov_b32_e32 v4, s0
	v_readlane_b32 s1, v254, 1
	s_cmpk_lt_i32 s30, 0x200
	s_waitcnt lgkmcnt(0)
	v_readfirstlane_b32 s16, v209
	v_readfirstlane_b32 s17, v208
	v_readfirstlane_b32 s10, v211
	v_readfirstlane_b32 s13, v210
	v_readfirstlane_b32 s1, v213
	v_readfirstlane_b32 s11, v212
	s_mov_b32 s0, s60
	s_cselect_b64 s[8:9], -1, 0
	s_cmpk_gt_i32 s30, 0x1ff
	v_readfirstlane_b32 s12, v8
	s_cbranch_scc1 .LBB0_154
	s_ashr_i32 s4, s30, 31
	s_lshr_b32 s4, s4, 29
	s_add_i32 s18, s30, s4
	s_and_b32 s4, s18, -8
	s_sub_i32 s19, s30, s4
	s_cmp_gt_i32 s19, -1
	s_mov_b64 s[4:5], -1
	s_cbranch_scc0 .LBB0_151
	s_lshl_b32 s20, s19, 6
	s_mov_b64 s[4:5], 0

.LBB0_207:
	v_lshl_add_u64 v[64:65], v[50:51], 0, s[6:7]
	global_load_dwordx4 v[56:59], v[64:65], off
	v_lshl_add_u64 v[66:67], v[48:49], 0, s[6:7]
	s_mov_b32 s2, 0x1000000
	v_add_co_u32_e32 v68, vcc, s2, v66
	s_mov_b32 s2, 0x1020000
	s_nop 0
	v_addc_co_u32_e32 v69, vcc, 0, v67, vcc
	global_load_dwordx4 v[60:63], v[68:69], off
	v_add_co_u32_e32 v70, vcc, s2, v66
	s_mov_b32 s2, 0x1040000
	s_nop 0
	v_addc_co_u32_e32 v71, vcc, 0, v67, vcc
	v_add_co_u32_e32 v66, vcc, s2, v66
	s_add_u32 s6, s6, 0x80
	s_nop 0
	v_addc_co_u32_e32 v67, vcc, 0, v67, vcc
	s_addc_u32 s7, s7, 0
	s_cmpk_lg_i32 s6, 0x200
	s_waitcnt vmcnt(0)
	v_mfma_f32_32x32x16_bf16 v[0:15], v[56:59], v[60:63], v[0:15]
	global_load_dwordx4 v[60:63], v[70:71], off
	s_waitcnt vmcnt(0)
	v_mfma_f32_32x32x16_bf16 v[16:31], v[56:59], v[60:63], v[16:31]
	global_load_dwordx4 v[60:63], v[66:67], off
	s_waitcnt vmcnt(0)
	v_mfma_f32_32x32x16_bf16 v[32:47], v[56:59], v[60:63], v[32:47]
	global_load_dwordx4 v[56:59], v[64:65], off offset:32
	global_load_dwordx4 v[60:63], v[68:69], off offset:32
	s_waitcnt vmcnt(0)
	v_mfma_f32_32x32x16_bf16 v[0:15], v[56:59], v[60:63], v[0:15]
	global_load_dwordx4 v[60:63], v[70:71], off offset:32
	s_waitcnt vmcnt(0)
	v_mfma_f32_32x32x16_bf16 v[16:31], v[56:59], v[60:63], v[16:31]
	global_load_dwordx4 v[60:63], v[66:67], off offset:32
	s_waitcnt vmcnt(0)
	v_mfma_f32_32x32x16_bf16 v[32:47], v[56:59], v[60:63], v[32:47]
	global_load_dwordx4 v[56:59], v[64:65], off offset:64
	global_load_dwordx4 v[60:63], v[68:69], off offset:64
	s_waitcnt vmcnt(0)
	v_mfma_f32_32x32x16_bf16 v[0:15], v[56:59], v[60:63], v[0:15]
	global_load_dwordx4 v[60:63], v[70:71], off offset:64
	s_waitcnt vmcnt(0)
	v_mfma_f32_32x32x16_bf16 v[16:31], v[56:59], v[60:63], v[16:31]
	global_load_dwordx4 v[60:63], v[66:67], off offset:64
	s_waitcnt vmcnt(0)
	v_mfma_f32_32x32x16_bf16 v[32:47], v[56:59], v[60:63], v[32:47]
	global_load_dwordx4 v[56:59], v[64:65], off offset:96
	global_load_dwordx4 v[60:63], v[68:69], off offset:96
	s_waitcnt vmcnt(0)
	v_mfma_f32_32x32x16_bf16 v[0:15], v[56:59], v[60:63], v[0:15]
	global_load_dwordx4 v[60:63], v[70:71], off offset:96
	s_waitcnt vmcnt(0)
	v_mfma_f32_32x32x16_bf16 v[16:31], v[56:59], v[60:63], v[16:31]
	global_load_dwordx4 v[60:63], v[66:67], off offset:96
	s_waitcnt vmcnt(0)
	v_mfma_f32_32x32x16_bf16 v[32:47], v[56:59], v[60:63], v[32:47]
	s_cbranch_scc1 .LBB0_207
	s_add_u32 s2, s9, 0x57327d00
	s_addc_u32 s9, s5, 0
	s_ashr_i32 s5, s4, 31
	s_lshl_b64 s[6:7], s[4:5], 15
	s_add_u32 s4, s8, 0x8003600
	s_addc_u32 s5, s1, 0
	s_movk_i32 s1, 0x60
	v_and_b32_e32 v48, 1, v55
	v_mul_lo_u32 v50, v53, s1
	s_add_u32 s6, s2, s6
	v_lshl_or_b32 v48, v48, 2, v50
	s_movk_i32 s2, 0x84
	v_lshlrev_b32_e32 v49, 2, v54
	v_mul_lo_u32 v48, v48, s2
	v_add3_u32 v48, 0, v49, v48
	ds_write2_b32 v48, v0, v1 offset1:33
	ds_write2_b32 v48, v2, v3 offset0:66 offset1:99
	v_add_u32_e32 v0, 0x400, v48
	ds_write2_b32 v0, v4, v5 offset0:8 offset1:41
	ds_write2_b32 v0, v6, v7 offset0:74 offset1:107
	v_add_u32_e32 v0, 0x800, v48
	ds_write2_b32 v0, v8, v9 offset0:16 offset1:49
	ds_write2_b32 v0, v10, v11 offset0:82 offset1:115
	v_add_u32_e32 v0, 0xc00, v48
	ds_write2_b32 v0, v12, v13 offset0:24 offset1:57
	ds_write2_b32 v0, v14, v15 offset0:90 offset1:123
	v_add_u32_e32 v0, 0x1000, v48
	ds_write2_b32 v0, v16, v17 offset0:32 offset1:65
	ds_write2_b32 v0, v18, v19 offset0:98 offset1:131
	v_add_u32_e32 v0, 0x1400, v48
	ds_write2_b32 v0, v20, v21 offset0:40 offset1:73
	ds_write2_b32 v0, v22, v23 offset0:106 offset1:139
	v_add_u32_e32 v0, 0x1800, v48
	ds_write2_b32 v0, v24, v25 offset0:48 offset1:81
	ds_write2_b32 v0, v26, v27 offset0:114 offset1:147
	v_add_u32_e32 v0, 0x1c00, v48
	ds_write2_b32 v0, v28, v29 offset0:56 offset1:89
	ds_write2_b32 v0, v30, v31 offset0:122 offset1:155
	v_add_u32_e32 v0, 0x2000, v48
	ds_write2_b32 v0, v32, v33 offset0:64 offset1:97
	ds_write2_b32 v0, v34, v35 offset0:130 offset1:163
	v_add_u32_e32 v0, 0x2400, v48
	s_addc_u32 s7, s9, s7
	ds_write2_b32 v0, v36, v37 offset0:72 offset1:105
	ds_write2_b32 v0, v38, v39 offset0:138 offset1:171
	v_add_u32_e32 v0, 0x2800, v48
	v_ashrrev_i32_e32 v2, 4, v52
	s_ashr_i32 s1, s0, 31
	ds_write2_b32 v0, v40, v41 offset0:80 offset1:113
	ds_write2_b32 v0, v42, v43 offset0:146 offset1:179
	v_add_u32_e32 v0, 0x2c00, v48
	s_lshl_b64 s[0:1], s[0:1], 5
	v_ashrrev_i32_e32 v3, 31, v2
	ds_write2_b32 v0, v44, v45 offset0:88 offset1:121
	ds_write2_b32 v0, v46, v47 offset0:154 offset1:187
	v_lshl_add_u64 v[0:1], s[0:1], 0, v[2:3]
	v_lshl_add_u64 v[4:5], v[0:1], 2, s[6:7]
	s_waitcnt lgkmcnt(0)
	s_barrier
	flat_load_dword v3, v[4:5]
	v_and_b32_e32 v5, 15, v52
	v_mov_b32_e32 v4, 0x60
	v_mov_b32_e32 v7, 0x120
	v_mul_u32_u24_e32 v40, 6, v5
	v_mad_u32_u24 v4, v5, 6, v4
	v_mov_b32_e32 v6, 0xc0
	v_mad_u32_u24 v7, v5, 6, v7
	v_mov_b32_e32 v9, 0x240
	v_mad_u32_u24 v6, v5, 6, v6
	v_mad_u32_u24 v9, v5, 6, v9
	v_and_b32_e32 v10, 30, v40
	v_and_b32_e32 v4, 0xe0, v4
	v_and_b32_e32 v7, 0x1e0, v7
	v_and_b32_e32 v11, 0x60, v40
	v_and_b32_e32 v12, 0x1e0, v6
	v_and_b32_e32 v18, 0x2e0, v9
	v_lshl_add_u32 v6, v10, 2, 0
	v_add_u32_e32 v4, v4, v2
	v_add_u32_e32 v7, v7, v2
	v_add_u32_e32 v9, v11, v2
	v_mad_u64_u32 v[10:11], s[0:1], v4, s2, v[6:7]
	v_mov_b32_e32 v8, 0x1e0
	v_mad_u32_u24 v8, v5, 6, v8
	v_and_b32_e32 v8, 0x3e0, v8
	v_add_u32_e32 v12, v12, v2
	v_add_u32_e32 v16, v8, v2
	v_mad_u64_u32 v[8:9], s[0:1], v9, s2, v[6:7]
	v_mad_u64_u32 v[12:13], s[0:1], v12, s2, v[6:7]
	v_mad_u64_u32 v[14:15], s[0:1], v7, s2, v[6:7]
	v_mad_u64_u32 v[16:17], s[0:1], v16, s2, v[6:7]
	v_add_u32_e32 v32, 0xc600, v8
	v_lshlrev_b32_e32 v144, 1, v40
	s_waitcnt vmcnt(0) lgkmcnt(0)
	v_fmamk_f32 v3, v3, 0x3a000000, v204
	v_rsq_f32_e32 v4, v3
	v_add_u32_e32 v3, v18, v2
	v_mad_u64_u32 v[18:19], s[0:1], v3, s2, v[6:7]
	v_mov_b32_e32 v3, 0x2a0
	v_mad_u32_u24 v3, v5, 6, v3
	v_and_b32_e32 v3, 0x3e0, v3
	v_add_u32_e32 v3, v3, v2
	v_mad_u64_u32 v[20:21], s[0:1], v3, s2, v[6:7]
	v_mov_b32_e32 v3, 0x61
	v_mad_u32_u24 v3, v5, 6, v3
	v_and_b32_e32 v3, 0xe0, v3
	v_add_u32_e32 v3, v3, v2
	v_mad_u64_u32 v[22:23], s[0:1], v3, s2, v[6:7]
	v_mov_b32_e32 v3, 0xc1
	v_mad_u32_u24 v3, v5, 6, v3
	v_and_b32_e32 v3, 0x1e0, v3
	v_add_u32_e32 v3, v3, v2
	v_mad_u64_u32 v[24:25], s[0:1], v3, s2, v[6:7]
	v_mov_b32_e32 v3, 0x121
	v_mad_u32_u24 v3, v5, 6, v3
	v_and_b32_e32 v3, 0x1e0, v3
	v_add_u32_e32 v3, v3, v2
	v_mad_u64_u32 v[26:27], s[0:1], v3, s2, v[6:7]
	v_mov_b32_e32 v3, 0x1e1
	v_mad_u32_u24 v3, v5, 6, v3
	v_and_b32_e32 v3, 0x3e0, v3
	v_add_u32_e32 v3, v3, v2
	v_mad_u64_u32 v[28:29], s[0:1], v3, s2, v[6:7]
	v_mov_b32_e32 v3, 0x241
	v_mad_u32_u24 v3, v5, 6, v3
	v_and_b32_e32 v3, 0x2e0, v3
	v_add_u32_e32 v3, v3, v2
	v_mad_u64_u32 v[30:31], s[0:1], v3, s2, v[6:7]
	v_mov_b32_e32 v3, 0x2a1
	v_mad_u32_u24 v3, v5, 6, v3
	v_and_b32_e32 v3, 0x3e0, v3
	v_add_u32_e32 v3, v3, v2
	v_mad_u64_u32 v[6:7], s[0:1], v3, s2, v[6:7]
	ds_read_b32 v10, v10
	ds_read_b32 v12, v12
	ds_read_b32 v14, v14
	ds_read2_b32 v[8:9], v8 offset1:1
	ds_read_b32 v16, v16
	ds_read_b32 v18, v18
	ds_read_b32 v20, v20
	ds_read_b32 v11, v22 offset:4
	ds_read_b32 v13, v24 offset:4
	ds_read_b32 v15, v26 offset:4
	ds_read_b32 v17, v28 offset:4
	ds_read2_b32 v[22:23], v32 offset1:1
	v_mad_u32_u24 v3, v5, 6, 2
	s_waitcnt lgkmcnt(8)
	v_pk_add_f32 v[8:9], v[8:9], 0 op_sel_hi:[1,0]
	v_and_b32_e32 v7, 30, v3
	v_and_b32_e32 v3, 0xe0, v3
	s_waitcnt lgkmcnt(4)
	v_pk_add_f32 v[8:9], v[8:9], v[10:11]
	v_lshl_add_u32 v10, v7, 2, 0
	v_add_u32_e32 v3, v3, v2
	s_waitcnt lgkmcnt(3)
	v_pk_add_f32 v[8:9], v[8:9], v[12:13]
	v_mad_u64_u32 v[12:13], s[0:1], v3, s2, v[10:11]
	v_mov_b32_e32 v3, 0x62
	v_mad_u32_u24 v3, v5, 6, v3
	v_and_b32_e32 v3, 0xe0, v3
	v_add_u32_e32 v3, v3, v2
	s_waitcnt lgkmcnt(2)
	v_pk_add_f32 v[8:9], v[8:9], v[14:15]
	v_mad_u64_u32 v[14:15], s[0:1], v3, s2, v[10:11]
	v_mov_b32_e32 v3, 0xc2
	v_mad_u32_u24 v3, v5, 6, v3
	v_and_b32_e32 v3, 0x1e0, v3
	s_waitcnt lgkmcnt(0)
	v_pk_add_f32 v[8:9], v[8:9], v[22:23]
	v_add_u32_e32 v3, v3, v2
	v_pk_add_f32 v[8:9], v[8:9], v[16:17]
	v_mad_u64_u32 v[16:17], s[0:1], v3, s2, v[10:11]
	v_mov_b32_e32 v3, 0x122
	v_mad_u32_u24 v3, v5, 6, v3
	v_and_b32_e32 v3, 0x1e0, v3
	v_add_u32_e32 v3, v3, v2
	v_mad_u64_u32 v[22:23], s[0:1], v3, s2, v[10:11]
	v_mov_b32_e32 v3, 0x182
	v_mad_u32_u24 v3, v5, 6, v3
	v_and_b32_e32 v3, 0x3e0, v3
	v_add_u32_e32 v3, v3, v2
	v_mad_u64_u32 v[24:25], s[0:1], v3, s2, v[10:11]
	v_mov_b32_e32 v3, 0x1e2
	v_mad_u32_u24 v3, v5, 6, v3
	v_and_b32_e32 v3, 0x3e0, v3
	v_add_u32_e32 v3, v3, v2
	v_mad_u64_u32 v[26:27], s[0:1], v3, s2, v[10:11]
	v_mov_b32_e32 v3, 0x242
	v_mad_u32_u24 v3, v5, 6, v3
	v_and_b32_e32 v3, 0x2e0, v3
	ds_read_b32 v19, v30 offset:4
	ds_read_b32 v21, v6 offset:4
	ds_read_b32 v6, v12
	ds_read_b32 v12, v14
	ds_read_b32 v14, v16
	ds_read_b32 v16, v22
	ds_read_b32 v22, v24
	ds_read_b32 v24, v26
	v_add_u32_e32 v3, v3, v2
	s_waitcnt lgkmcnt(7)
	v_pk_add_f32 v[8:9], v[8:9], v[18:19]
	v_mad_u64_u32 v[18:19], s[0:1], v3, s2, v[10:11]
	v_mov_b32_e32 v3, 0x2a2
	v_mad_u32_u24 v3, v5, 6, v3
	v_and_b32_e32 v3, 0x3e0, v3
	v_add_u32_e32 v3, v3, v2
	v_mad_u64_u32 v[10:11], s[0:1], v3, s2, v[10:11]
	v_mad_u32_u24 v3, v5, 6, 3
	v_and_b32_e32 v7, 31, v3
	v_and_b32_e32 v3, 0xe0, v3
	s_waitcnt lgkmcnt(6)
	v_pk_add_f32 v[8:9], v[8:9], v[20:21]
	v_lshl_add_u32 v20, v7, 2, 0
	v_add_u32_e32 v3, v3, v2
	v_mad_u64_u32 v[26:27], s[0:1], v3, s2, v[20:21]
	v_mov_b32_e32 v3, 0x63
	v_mad_u32_u24 v3, v5, 6, v3
	v_and_b32_e32 v3, 0xe0, v3
	v_add_u32_e32 v3, v3, v2
	v_mad_u64_u32 v[28:29], s[0:1], v3, s2, v[20:21]
	v_mov_b32_e32 v3, 0xc3
	v_mad_u32_u24 v3, v5, 6, v3
	v_and_b32_e32 v3, 0x1e0, v3
	v_add_u32_e32 v3, v3, v2
	v_mad_u64_u32 v[30:31], s[0:1], v3, s2, v[20:21]
	v_mov_b32_e32 v3, 0x123
	v_mad_u32_u24 v3, v5, 6, v3
	v_and_b32_e32 v3, 0x1e0, v3
	v_add_u32_e32 v3, v3, v2
	v_mad_u64_u32 v[32:33], s[0:1], v3, s2, v[20:21]
	v_mov_b32_e32 v3, 0x183
	v_mad_u32_u24 v3, v5, 6, v3
	v_and_b32_e32 v3, 0x3e0, v3
	v_add_u32_e32 v3, v3, v2
	v_mad_u64_u32 v[34:35], s[0:1], v3, s2, v[20:21]
	v_mov_b32_e32 v3, 0x1e3
	v_mad_u32_u24 v3, v5, 6, v3
	v_and_b32_e32 v3, 0x3e0, v3
	v_add_u32_e32 v3, v3, v2
	v_mad_u64_u32 v[36:37], s[0:1], v3, s2, v[20:21]
	v_mov_b32_e32 v3, 0x243
	v_mad_u32_u24 v3, v5, 6, v3
	v_and_b32_e32 v3, 0x2e0, v3
	v_add_u32_e32 v3, v3, v2
	ds_read_b32 v18, v18
	ds_read_b32 v10, v10
	ds_read_b32 v7, v26
	ds_read_b32 v13, v28
	ds_read_b32 v15, v30
	ds_read_b32 v17, v32
	ds_read_b32 v23, v34
	ds_read_b32 v25, v36
	v_mad_u64_u32 v[26:27], s[0:1], v3, s2, v[20:21]
	v_mov_b32_e32 v3, 0x2a3
	v_mad_u32_u24 v3, v5, 6, v3
	v_and_b32_e32 v3, 0x3e0, v3
	v_add_u32_e32 v3, v3, v2
	v_mad_u64_u32 v[20:21], s[0:1], v3, s2, v[20:21]
	v_mad_u32_u24 v3, v5, 6, 4
	s_waitcnt lgkmcnt(5)
	v_pk_add_f32 v[6:7], v[6:7], 0 op_sel_hi:[1,0]
	v_and_b32_e32 v11, 30, v3
	v_and_b32_e32 v3, 0xe0, v3
	s_waitcnt lgkmcnt(4)
	v_pk_add_f32 v[6:7], v[6:7], v[12:13]
	v_lshl_add_u32 v12, v11, 2, 0
	v_add_u32_e32 v3, v3, v2
	s_waitcnt lgkmcnt(3)
	v_pk_add_f32 v[6:7], v[6:7], v[14:15]
	v_mad_u64_u32 v[14:15], s[0:1], v3, s2, v[12:13]
	v_mov_b32_e32 v3, 0x64
	v_mad_u32_u24 v3, v5, 6, v3
	v_and_b32_e32 v3, 0xe0, v3
	v_add_u32_e32 v3, v3, v2
	s_waitcnt lgkmcnt(2)
	v_pk_add_f32 v[6:7], v[6:7], v[16:17]
	v_mad_u64_u32 v[16:17], s[0:1], v3, s2, v[12:13]
	v_mov_b32_e32 v3, 0xc4
	v_mad_u32_u24 v3, v5, 6, v3
	v_and_b32_e32 v3, 0x1e0, v3
	v_add_u32_e32 v3, v3, v2
	s_waitcnt lgkmcnt(1)
	v_pk_add_f32 v[6:7], v[6:7], v[22:23]
	v_mad_u64_u32 v[22:23], s[0:1], v3, s2, v[12:13]
	v_mov_b32_e32 v3, 0x124
	v_mad_u32_u24 v3, v5, 6, v3
	v_and_b32_e32 v3, 0x1e0, v3
	v_add_u32_e32 v3, v3, v2
	s_waitcnt lgkmcnt(0)
	v_pk_add_f32 v[6:7], v[6:7], v[24:25]
	v_mad_u64_u32 v[24:25], s[0:1], v3, s2, v[12:13]
	v_mov_b32_e32 v3, 0x184
	v_mad_u32_u24 v3, v5, 6, v3
	v_and_b32_e32 v3, 0x3e0, v3
	v_add_u32_e32 v3, v3, v2
	v_mad_u64_u32 v[28:29], s[0:1], v3, s2, v[12:13]
	v_mov_b32_e32 v3, 0x1e4
	v_mad_u32_u24 v3, v5, 6, v3
	v_and_b32_e32 v3, 0x3e0, v3
	v_add_u32_e32 v3, v3, v2
	v_mad_u64_u32 v[30:31], s[0:1], v3, s2, v[12:13]
	v_mov_b32_e32 v3, 0x244
	v_mad_u32_u24 v3, v5, 6, v3
	v_and_b32_e32 v3, 0x2e0, v3
	ds_read_b32 v19, v26
	ds_read_b32 v11, v20
	ds_read_b32 v14, v14
	ds_read_b32 v16, v16
	ds_read_b32 v20, v22
	ds_read_b32 v22, v24
	ds_read_b32 v24, v28
	ds_read_b32 v26, v30
	s_waitcnt lgkmcnt(7)
	v_pk_add_f32 v[6:7], v[6:7], v[18:19]
	v_add_u32_e32 v3, v3, v2
	s_waitcnt lgkmcnt(6)
	v_pk_add_f32 v[6:7], v[6:7], v[10:11]
	v_mad_u64_u32 v[10:11], s[0:1], v3, s2, v[12:13]
	v_mov_b32_e32 v3, 0x2a4
	v_mad_u32_u24 v3, v5, 6, v3
	v_and_b32_e32 v3, 0x3e0, v3
	v_add_u32_e32 v3, v3, v2
	v_mad_u64_u32 v[12:13], s[0:1], v3, s2, v[12:13]
	v_mad_u32_u24 v3, v5, 6, 5
	v_and_b32_e32 v11, 31, v3
	v_and_b32_e32 v3, 0xe0, v3
	v_lshl_add_u32 v18, v11, 2, 0
	v_add_u32_e32 v3, v3, v2
	v_mad_u64_u32 v[28:29], s[0:1], v3, s2, v[18:19]
	v_mov_b32_e32 v3, 0x65
	v_mad_u32_u24 v3, v5, 6, v3
	v_and_b32_e32 v3, 0xe0, v3
	v_add_u32_e32 v3, v3, v2
	v_mad_u64_u32 v[30:31], s[0:1], v3, s2, v[18:19]
	v_mov_b32_e32 v3, 0xc5
	v_mad_u32_u24 v3, v5, 6, v3
	v_and_b32_e32 v3, 0x1e0, v3
	v_add_u32_e32 v3, v3, v2
	v_mad_u64_u32 v[32:33], s[0:1], v3, s2, v[18:19]
	v_mov_b32_e32 v3, 0x125
	v_mad_u32_u24 v3, v5, 6, v3
	v_and_b32_e32 v3, 0x1e0, v3
	v_add_u32_e32 v3, v3, v2
	v_mad_u64_u32 v[34:35], s[0:1], v3, s2, v[18:19]
	v_mov_b32_e32 v3, 0x185
	v_mad_u32_u24 v3, v5, 6, v3
	v_and_b32_e32 v3, 0x3e0, v3
	v_add_u32_e32 v3, v3, v2
	v_mad_u64_u32 v[36:37], s[0:1], v3, s2, v[18:19]
	v_mov_b32_e32 v3, 0x1e5
	v_mad_u32_u24 v3, v5, 6, v3
	v_and_b32_e32 v3, 0x3e0, v3
	v_add_u32_e32 v3, v3, v2
	v_mad_u64_u32 v[38:39], s[0:1], v3, s2, v[18:19]
	v_mov_b32_e32 v3, 0x245
	v_mad_u32_u24 v3, v5, 6, v3
	v_and_b32_e32 v3, 0x2e0, v3
	v_add_u32_e32 v3, v3, v2
	ds_read_b32 v10, v10
	ds_read_b32 v12, v12
	ds_read_b32 v15, v28
	ds_read_b32 v17, v30
	ds_read_b32 v21, v32
	ds_read_b32 v23, v34
	ds_read_b32 v25, v36
	ds_read_b32 v27, v38
	v_mad_u64_u32 v[28:29], s[0:1], v3, s2, v[18:19]
	v_mov_b32_e32 v3, 0x2a5
	v_mad_u32_u24 v3, v5, 6, v3
	v_and_b32_e32 v3, 0x3e0, v3
	v_add_u32_e32 v2, v3, v2
	v_mad_u64_u32 v[2:3], s[0:1], v2, s2, v[18:19]
	ds_read_b32 v11, v28
	ds_read_b32 v13, v2
	s_waitcnt lgkmcnt(7)
	v_pk_add_f32 v[2:3], v[14:15], 0 op_sel_hi:[1,0]
	v_pk_mul_f32 v[8:9], v[4:5], v[8:9] op_sel_hi:[0,1]
	s_waitcnt lgkmcnt(6)
	v_pk_add_f32 v[2:3], v[2:3], v[16:17]
	v_pk_mul_f32 v[6:7], v[4:5], v[6:7] op_sel_hi:[0,1]
	s_waitcnt lgkmcnt(5)
	v_pk_add_f32 v[2:3], v[2:3], v[20:21]
	s_waitcnt lgkmcnt(4)
	v_pk_add_f32 v[2:3], v[2:3], v[22:23]
	s_waitcnt lgkmcnt(3)
	v_pk_add_f32 v[2:3], v[2:3], v[24:25]
	s_waitcnt lgkmcnt(2)
	v_pk_add_f32 v[2:3], v[2:3], v[26:27]
	s_waitcnt lgkmcnt(1)
	v_pk_add_f32 v[2:3], v[2:3], v[10:11]
	s_waitcnt lgkmcnt(0)
	v_pk_add_f32 v[2:3], v[2:3], v[12:13]
	s_nop 0
	v_pk_mul_f32 v[2:3], v[4:5], v[2:3] op_sel_hi:[0,1]
	v_mov_b64_e32 v[4:5], s[4:5]
	v_mad_u64_u32 v[4:5], s[0:1], v0, s80, v[4:5]
	v_mad_i32_i24 v5, v1, s80, v5
	v_lshl_add_u64 v[4:5], v[4:5], 0, v[144:145]
	v_add_co_u32_e32 v4, vcc, s55, v4
	v_cvt_pk_bf16_f32 v0, v8, v9
	v_cvt_pk_bf16_f32 v1, v6, v7
	v_cvt_pk_bf16_f32 v2, v2, v3
	v_addc_co_u32_e32 v5, vcc, 0, v5, vcc
	s_mov_b32 s0, s37
	global_store_dwordx3 v[4:5], v[0:2], off
	s_barrier
	s_mov_b32 s1, s33
	v_mbcnt_lo_u32_b32 v0, -1, s0
	v_mbcnt_hi_u32_b32 v0, -1, v0
	v_lshl_or_b32 v8, s1, 6, v0
	v_readlane_b32 s0, v254, 0
	s_mov_b32 s10, s0
	s_mov_b32 s0, s37
	v_readlane_b32 s1, v254, 1
	s_add_i32 s0, s0, 0x20120
	v_mov_b32_e32 v0, s0
	s_mov_b32 s0, s60
	s_mov_b32 s1, 0
	v_mov_b32_e32 v251, 0x20000
	ds_read_b64 v[206:207], v251 offset:288
	ds_read_b64 v[208:209], v251 offset:288
	ds_read_b64 v[210:211], v251 offset:288
	s_add_i32 s1, s1, 0x20120
	v_mov_b32_e32 v2, s1
	s_mov_b32 s4, s60
	s_mov_b32 s1, 0
	s_add_i32 s1, s1, 0x20120
	v_mov_b32_e32 v4, s1
	s_waitcnt lgkmcnt(2)
	v_readfirstlane_b32 s1, v207
	v_readfirstlane_b32 s14, v206
	s_waitcnt lgkmcnt(1)
	v_readfirstlane_b32 s5, v209
	v_readfirstlane_b32 s12, v208
	s_waitcnt lgkmcnt(0)
	v_readfirstlane_b32 s2, v211
	v_readfirstlane_b32 s9, v210
	s_cmpk_gt_i32 s10, 0xff
	v_readfirstlane_b32 s8, v8
	s_cbranch_scc1 .LBB0_230
	s_ashr_i32 s11, s10, 31
	s_lshr_b32 s6, s11, 29
	s_add_i32 s16, s10, s6
	s_and_b32 s6, s16, -8
	s_sub_i32 s15, s10, s6
	s_cmp_gt_i32 s15, -1
	s_mov_b64 s[6:7], -1
	s_cbranch_scc0 .LBB0_211
	s_lshl_b32 s13, s15, 5
	s_mov_b64 s[6:7], 0

.LBB0_274:
	s_or_b64 exec, exec, s[64:65]
	s_mov_b32 s0, s37
	s_waitcnt lgkmcnt(0)
	s_barrier
	s_mov_b32 s1, s33
	v_mbcnt_lo_u32_b32 v0, -1, s0
	v_mbcnt_hi_u32_b32 v0, -1, v0
	v_lshl_or_b32 v1, s1, 6, v0
	v_readlane_b32 s0, v254, 0
	s_mov_b32 s29, s0
	s_mov_b32 s0, s37
	s_add_i32 s0, s0, 0x20120
	v_mov_b32_e32 v0, s0
	v_mov_b32_e32 v251, 0x20000
	ds_read_b64 v[206:207], v251 offset:288
	ds_read_b64 v[208:209], v251 offset:56
	ds_read_b64 v[210:211], v251 offset:288
	ds_read_b64 v[212:213], v251 offset:288
	ds_read_b64 v[214:215], v251 offset:288
	ds_read_b64 v[216:217], v251 offset:288
	ds_read_b64 v[218:219], v251 offset:288
	ds_read_b64 v[224:225], v251 offset:288
	ds_read_b64 v[226:227], v251 offset:288
	s_mov_b32 s0, 0
	s_add_i32 s0, s0, 0x20038
	v_mov_b32_e32 v0, s0
	s_waitcnt lgkmcnt(0)
	v_readfirstlane_b32 s4, v207
	v_readfirstlane_b32 s5, v206
	s_mov_b32 s2, s60
	s_mov_b32 s6, 0
	s_add_i32 s6, s6, 0x20120
	v_readlane_b32 s1, v254, 1
	v_mov_b32_e32 v0, s6
	s_waitcnt lgkmcnt(0)
	v_readfirstlane_b32 s0, v209
	v_readfirstlane_b32 s1, v208
	s_mov_b32 s8, 0
	s_add_i32 s8, s8, 0x20120
	v_mov_b32_e32 v0, s8
	s_waitcnt lgkmcnt(0)
	v_readfirstlane_b32 s6, v211
	v_readfirstlane_b32 s7, v210
	s_mov_b32 s10, 0
	s_add_i32 s10, s10, 0x20120
	v_mov_b32_e32 v0, s10
	s_waitcnt lgkmcnt(0)
	v_readfirstlane_b32 s8, v213
	v_readfirstlane_b32 s9, v212
	s_mov_b32 s12, 0
	s_add_i32 s12, s12, 0x20120
	v_mov_b32_e32 v0, s12
	s_waitcnt lgkmcnt(0)
	v_readfirstlane_b32 s10, v215
	v_readfirstlane_b32 s11, v214
	s_mov_b32 s12, 0
	s_add_i32 s12, s12, 0x20120
	v_mov_b32_e32 v0, s12
	s_waitcnt lgkmcnt(0)
	v_readfirstlane_b32 s14, v217
	v_readfirstlane_b32 s15, v216
	s_mov_b32 s16, 0
	s_add_i32 s16, s16, 0x20120
	v_mov_b32_e32 v0, s16
	s_waitcnt lgkmcnt(0)
	v_readfirstlane_b32 s12, v219
	v_readfirstlane_b32 s13, v218
	s_mov_b32 s16, 0
	s_add_i32 s16, s16, 0x20120
	v_mov_b32_e32 v0, s16
	s_waitcnt lgkmcnt(0)
	v_readfirstlane_b32 s30, v225
	v_readfirstlane_b32 s31, v224
	v_ashrrev_i32_e32 v0, 6, v1
	s_lshl_b32 s28, s29, 3
	v_add_u32_e32 v42, s28, v0
	v_cmp_gt_i32_e32 vcc, s55, v42
	s_waitcnt lgkmcnt(0)
	v_readfirstlane_b32 s34, v227
	v_readfirstlane_b32 s35, v226
	s_and_saveexec_b64 s[16:17], vcc
	s_cbranch_execz .LBB0_295
	s_add_u32 s26, s5, 0x8003600
	s_addc_u32 s27, s4, 0
	s_add_u32 s18, s7, 0x1a5cb600
	s_addc_u32 s19, s6, 0
	s_add_u32 s20, s9, 0x1a60b600
	s_addc_u32 s21, s8, 0
	s_add_u32 s22, s11, 0x1a64b600
	s_addc_u32 s23, s10, 0
	s_add_u32 s24, s15, 0x1a6cb600
	s_addc_u32 s25, s14, 0
	v_and_b32_e32 v8, 63, v1
	s_add_u32 s38, s31, 0x5733fd00
	v_cmp_gt_u32_e32 vcc, 9, v8
	v_mov_b32_e32 v4, 0x3e38aa3b
	s_addc_u32 s39, s30, 0
	v_cndmask_b32_e32 v12, 1.0, v4, vcc
	v_mul_lo_u16_e32 v4, 0xab, v8
	s_add_u32 s30, s35, 0x57347d00
	v_lshrrev_b16_e32 v4, 10, v4
	s_addc_u32 s31, s34, 0
	v_mul_lo_u16_e32 v5, 6, v4
	s_add_u32 s34, s13, 0x4cb9fd00
	v_sub_u16_e32 v6, v8, v5
	s_addc_u32 s35, s12, 0
	s_mul_hi_i32 s4, s2, 0x1500
	s_mulk_i32 s2, 0x1500
	v_lshlrev_b16_e32 v9, 3, v6
	v_lshlrev_b32_e32 v6, 2, v8
	s_add_u32 s44, s1, s2
	v_xor_b32_e32 v43, 0x80, v6
	v_xor_b32_e32 v44, 64, v6
	v_xor_b32_e32 v45, 32, v6
	v_xor_b32_e32 v46, 16, v6
	v_xor_b32_e32 v47, 8, v6
	v_xor_b32_e32 v48, 4, v6
	v_lshlrev_b32_e32 v6, 3, v0
	s_addc_u32 s45, s0, s4
	v_lshlrev_b32_e32 v1, 3, v8
	v_lshl_add_u32 v16, s29, 6, v6
	s_lshl_b32 s2, s29, 7
	v_lshlrev_b32_e32 v6, 4, v0
	v_add3_u32 v18, s2, v6, v1
	v_ashrrev_i32_e32 v1, 31, v0
	s_ashr_i32 s29, s28, 31
	v_lshlrev_b32_e32 v144, 5, v8
	v_lshl_add_u64 v[0:1], v[0:1], 0, s[28:29]
	v_lshl_add_u64 v[14:15], s[44:45], 0, v[144:145]
	v_lshlrev_b64 v[6:7], 12, v[0:1]
	v_lshlrev_b32_e32 v144, 4, v8
	v_or_b32_e32 v6, v6, v144
	v_lshl_add_u64 v[20:21], s[34:35], 0, v[6:7]
	v_lshlrev_b64 v[6:7], 2, v[0:1]
	v_lshl_add_u64 v[22:23], s[38:39], 0, v[6:7]
	v_lshl_add_u64 v[24:25], s[30:31], 0, v[6:7]
	v_mov_b64_e32 v[6:7], s[26:27]
	v_lshlrev_b32_e32 v2, 6, v8
	v_mad_u64_u32 v[26:27], s[26:27], v0, s80, v[6:7]
	v_add_u32_e32 v3, 0xfffffdc0, v2
	v_mad_i32_i24 v27, v1, s80, v27
	v_mov_b32_e32 v0, 0x1280
	v_mov_b32_e32 v1, 0xe00
	v_cndmask_b32_e32 v2, v3, v2, vcc
	v_mov_b32_e32 v3, v145
	v_cndmask_b32_e32 v0, v0, v1, vcc
	v_mov_b32_e32 v1, v145
	v_lshl_add_u64 v[28:29], v[2:3], 1, v[0:1]
	v_and_b32_e32 v0, 0xf8, v9
	v_lshlrev_b32_e32 v4, 7, v4
	v_mov_b32_e32 v5, v145
	v_lshlrev_b32_e32 v0, 1, v0
	v_lshl_add_u64 v[0:1], v[4:5], 0, v[0:1]
	s_mov_b64 s[26:27], 0xe20
	v_cmp_gt_u32_e64 s[0:1], 56, v8
	v_cmp_gt_u32_e64 s[4:5], 18, v8
	v_cmp_gt_u32_e64 s[6:7], 54, v8
	v_cmp_gt_u32_e64 s[8:9], 2, v8
	v_cmp_gt_u32_e64 s[10:11], 48, v8
	v_cmp_gt_u32_e64 s[12:13], 32, v8
	v_cmp_eq_u32_e64 s[14:15], 0, v8
	v_mov_b32_e32 v13, v12
	v_or_b32_e32 v28, 16, v28
	v_lshl_add_u64 v[30:31], v[0:1], 0, s[26:27]
	s_mov_b64 s[26:27], 0
	s_branch .LBB0_277

.LBB0_295:
	s_or_b64 exec, exec, s[16:17]
	s_mov_b32 s0, s37
	s_mov_b32 s1, s33
	v_mbcnt_lo_u32_b32 v0, -1, s0
	v_mbcnt_hi_u32_b32 v0, -1, v0
	v_lshl_or_b32 v0, s1, 6, v0
	v_readlane_b32 s0, v254, 0
	s_mov_b32 s8, s0
	s_mov_b32 s0, s37
	s_add_i32 s0, s0, 0x20120
	v_mov_b32_e32 v1, s0
	v_readlane_b32 s1, v254, 1
	s_waitcnt lgkmcnt(0)
	v_mov_b32_e32 v251, 0x20000
	ds_read_b64 v[206:207], v251 offset:288
	ds_read_b64 v[208:209], v251 offset:64
	ds_read_b64 v[210:211], v251 offset:72
	ds_read_b64 v[212:213], v251 offset:80
	ds_read_b64 v[214:215], v251 offset:88
	ds_read_b64 v[216:217], v251 offset:96
	ds_read_b64 v[218:219], v251 offset:288
	s_mov_b32 s1, 0
	s_add_i32 s1, s1, 0x20040
	v_mov_b32_e32 v1, s1
	s_waitcnt lgkmcnt(0)
	v_readfirstlane_b32 s0, v207
	v_readfirstlane_b32 s2, v206
	s_mov_b32 s6, s60
	s_mov_b32 s5, 0
	s_add_i32 s5, s5, 0x20048
	v_mov_b32_e32 v1, s5
	s_waitcnt lgkmcnt(0)
	v_readfirstlane_b32 s1, v209
	v_readfirstlane_b32 s4, v208
	s_mov_b32 s14, s60
	s_mov_b32 s9, 0
	s_add_i32 s9, s9, 0x20050
	v_mov_b32_e32 v1, s9
	s_waitcnt lgkmcnt(0)
	v_readfirstlane_b32 s5, v211
	v_readfirstlane_b32 s7, v210
	s_mov_b32 s18, s60
	s_mov_b32 s9, 0
	s_add_i32 s9, s9, 0x20058
	v_mov_b32_e32 v1, s9
	s_waitcnt lgkmcnt(0)
	v_readfirstlane_b32 s17, v213
	v_readfirstlane_b32 s16, v212
	s_mov_b32 s22, s60
	s_mov_b32 s9, 0
	s_add_i32 s9, s9, 0x20060
	v_mov_b32_e32 v1, s9
	s_waitcnt lgkmcnt(0)
	v_readfirstlane_b32 s19, v215
	v_readfirstlane_b32 s20, v214
	s_mov_b32 s24, s60
	s_mov_b32 s9, 0
	s_add_i32 s9, s9, 0x20120
	v_mov_b32_e32 v1, s9
	s_waitcnt lgkmcnt(0)
	v_readfirstlane_b32 s21, v217
	v_readfirstlane_b32 s23, v216
	v_ashrrev_i32_e32 v1, 6, v0
	v_lshl_add_u32 v9, s8, 3, v1
	s_movk_i32 s8, 0xe00
	v_cmp_gt_i32_e32 vcc, s8, v9
	s_waitcnt lgkmcnt(0)
	v_readfirstlane_b32 s25, v219
	v_readfirstlane_b32 s26, v218
	s_and_saveexec_b64 s[8:9], vcc
	s_cbranch_execz .LBB0_308
	s_add_u32 s10, s2, 0x8003600
	s_addc_u32 s11, s0, 0
	s_mul_hi_i32 s0, s6, 0x1c00
	s_mulk_i32 s6, 0x1c00
	s_add_u32 s12, s4, s6
	s_addc_u32 s13, s1, s0
	s_mul_hi_i32 s0, s14, 0x1c00
	s_mulk_i32 s14, 0x1c00
	s_add_u32 s14, s7, s14
	s_addc_u32 s15, s5, s0
	s_mul_hi_i32 s0, s18, 0x70
	s_mulk_i32 s18, 0x70
	s_add_u32 s16, s16, s18
	s_addc_u32 s17, s17, s0
	s_mul_hi_i32 s0, s22, 0x1c000
	s_mul_i32 s22, s22, 0x1c000
	s_add_u32 s18, s20, s22
	s_addc_u32 s19, s19, s0
	s_mul_hi_i32 s0, s24, 0x1c000
	s_mul_i32 s24, s24, 0x1c000
	s_add_u32 s20, s23, s24
	s_addc_u32 s21, s21, s0
	v_and_b32_e32 v8, 63, v0
	s_add_u32 s22, s26, 0x1944b600
	v_lshl_add_u32 v54, v1, 11, 0
	v_lshlrev_b32_e32 v0, 5, v8
	s_addc_u32 s23, s25, 0
	v_mul_hi_u32_u24_e32 v11, 0x20c0, v8
	v_mul_u32_u24_e32 v10, 0x20c0, v8
	s_mov_b64 s[24:25], 0
	v_add_u32_e32 v55, v54, v0
	v_lshlrev_b32_e32 v144, 2, v8

.LBB0_352:
	s_or_b64 exec, exec, s[64:65]
	s_mov_b32 s0, s37
	s_waitcnt lgkmcnt(0)
	s_barrier
	s_mov_b32 s1, s33
	v_mbcnt_lo_u32_b32 v0, -1, s0
	v_mbcnt_hi_u32_b32 v0, -1, v0
	v_lshl_or_b32 v0, s1, 6, v0
	v_readlane_b32 s0, v254, 0
	s_mov_b32 s30, s0
	s_mov_b32 s0, s37
	s_add_i32 s0, s0, 0x20120
	v_mov_b32_e32 v1, s0
	v_mov_b32_e32 v251, 0x20000
	ds_read_b64 v[206:207], v251 offset:288
	ds_read_b64 v[208:209], v251 offset:288
	ds_read_b64 v[210:211], v251 offset:288
	s_mov_b32 s2, 0
	s_add_i32 s2, s2, 0x20120
	v_readlane_b32 s1, v254, 1
	v_mov_b32_e32 v1, s2
	s_waitcnt lgkmcnt(0)
	v_readfirstlane_b32 s0, v207
	v_readfirstlane_b32 s1, v206
	s_mov_b32 s5, 0
	s_add_i32 s5, s5, 0x20120
	v_mov_b32_e32 v1, s5
	s_waitcnt lgkmcnt(0)
	v_readfirstlane_b32 s2, v209
	v_readfirstlane_b32 s4, v208
	s_cmpk_gt_i32 s30, 0x23f
	s_waitcnt lgkmcnt(0)
	v_readfirstlane_b32 s5, v211
	v_readfirstlane_b32 s10, v210
	s_cbranch_scc1 .LBB0_369
	s_add_u32 s6, s1, 0x8003600
	s_addc_u32 s7, s0, 0
	s_add_u32 s8, s4, 0x18203600
	v_and_b32_e32 v81, 15, v0
	v_ashrrev_i32_e32 v91, 3, v0
	v_and_b32_e32 v1, 63, v0
	v_bfe_u32 v3, v0, 4, 2
	v_ashrrev_i32_e32 v2, 2, v0
	v_lshlrev_b32_e32 v4, 3, v0
	v_and_b32_e32 v0, 48, v0
	s_addc_u32 s9, s2, 0
	v_and_b32_e32 v4, 56, v4
	s_movk_i32 s0, 0x48
	v_add_u32_e32 v96, 0, v0
	v_lshlrev_b32_e32 v0, 2, v1
	s_add_u32 s10, s10, 0x19403600
	v_and_b32_e32 v94, -16, v2
	v_lshlrev_b32_e32 v2, 3, v3
	v_mad_u64_u32 v[6:7], s[0:1], v91, s0, v[4:5]
	v_lshlrev_b32_e32 v5, 1, v91
	v_lshlrev_b32_e32 v80, 2, v3
	v_xor_b32_e32 v98, 64, v0
	v_xor_b32_e32 v99, 0x80, v0
	v_mul_u32_u24_e32 v0, 0x88, v4
	s_addc_u32 s11, s5, 0
	v_lshl_add_u32 v95, v6, 1, 0
	v_add_u32_e32 v97, 0, v2
	v_cmp_gt_u32_e64 s[0:1], 16, v1
	s_and_b32 s31, s30, 3
	s_and_b32 s34, s30, 15
	s_bfe_u32 s36, s30, 0x20002
	v_add3_u32 v100, 0, v5, v0
	v_mul_u32_u24_e32 v101, 0x90, v81
	v_mul_u32_u24_e32 v102, 0x88, v81
	v_lshlrev_b32_e32 v82, 1, v2
	v_lshlrev_b32_e32 v144, 1, v4
	v_lshlrev_b32_e32 v84, 2, v80
	s_branch .LBB0_355

.LBB0_369:
	s_mov_b32 s0, s37
	s_mov_b32 s1, s33
	v_mbcnt_lo_u32_b32 v0, -1, s0
	v_mbcnt_hi_u32_b32 v0, -1, v0
	s_waitcnt vmcnt(0)
	v_lshl_or_b32 v8, s1, 6, v0
	v_readlane_b32 s0, v254, 0
	s_mov_b32 s26, s0
	s_cmpk_gt_i32 s26, 0x7f
	v_readlane_b32 s1, v254, 1
	s_cbranch_scc1 .LBB0_433
	s_mov_b32 s0, s37
	s_add_i32 s0, s0, 0x20120
	v_mov_b32_e32 v0, s0
	v_mov_b32_e32 v251, 0x20000
	ds_read_b64 v[206:207], v251 offset:288
	ds_read_b64 v[208:209], v251 offset:288
	ds_read_b64 v[210:211], v251 offset:288
	ds_read_b64 v[212:213], v251 offset:288
	s_mov_b32 s0, 0
	s_add_i32 s0, s0, 0x20120
	s_mov_b32 s13, s60
	s_waitcnt lgkmcnt(0)
	v_readfirstlane_b32 s7, v206
	v_mov_b32_e32 v0, s0
	v_readfirstlane_b32 s6, v207
	s_mov_b32 s0, 0
	s_add_i32 s0, s0, 0x20120
	s_waitcnt lgkmcnt(0)
	v_readfirstlane_b32 s12, v208
	v_mov_b32_e32 v0, s0
	v_readfirstlane_b32 s11, v209
	s_mov_b32 s0, 0
	s_add_i32 s0, s0, 0x20120
	s_ashr_i32 s27, s26, 31
	s_waitcnt lgkmcnt(0)
	v_readfirstlane_b32 s8, v210
	v_mov_b32_e32 v0, s0
	v_readfirstlane_b32 s5, v211
	s_lshr_b32 s0, s27, 29
	s_add_i32 s15, s26, s0
	s_and_b32 s0, s15, -8
	s_sub_i32 s14, s26, s0
	s_waitcnt lgkmcnt(0)
	v_readfirstlane_b32 s2, v213
	v_readfirstlane_b32 s10, v212
	v_readfirstlane_b32 s4, v8
	s_mov_b64 s[0:1], -1
	s_cmp_gt_i32 s14, -1
	s_cbranch_scc0 .LBB0_372
	s_lshl_b32 s9, s14, 4
	s_mov_b64 s[0:1], 0

.LBB0_487:
	s_mov_b32 s0, s37
	s_mov_b32 s1, s33
	v_mbcnt_lo_u32_b32 v0, -1, s0
	v_mbcnt_hi_u32_b32 v0, -1, v0
	v_lshl_or_b32 v8, s1, 6, v0
	v_readlane_b32 s0, v254, 0
	s_mov_b32 s5, s0
	s_cmpk_lt_i32 s5, 0xc0
	v_readlane_b32 s1, v254, 1
	s_cbranch_scc1 .LBB0_517
	s_mov_b32 s0, s37
	s_add_i32 s0, s0, 0x20120
	v_mov_b32_e32 v0, s0
	v_mov_b32_e32 v251, 0x20000
	ds_read_b64 v[206:207], v251 offset:288
	ds_read_b64 v[208:209], v251 offset:288
	ds_read_b64 v[210:211], v251 offset:288
	ds_read_b64 v[212:213], v251 offset:288
	s_mov_b32 s8, s60
	s_mov_b32 s0, 0
	s_add_i32 s0, s0, 0x20120
	s_waitcnt lgkmcnt(0)
	v_readfirstlane_b32 s7, v206
	v_mov_b32_e32 v0, s0
	v_readfirstlane_b32 s6, v207
	s_mov_b32 s0, 0
	s_add_i32 s0, s0, 0x20120
	s_add_i32 s34, s5, 0xffffff40
	s_waitcnt lgkmcnt(0)
	v_readfirstlane_b32 s11, v208
	v_mov_b32_e32 v0, s0
	v_readfirstlane_b32 s9, v209
	s_mov_b32 s0, 0
	s_add_i32 s0, s0, 0x20120
	s_cmpk_gt_u32 s34, 0x5f
	s_waitcnt lgkmcnt(0)
	v_readfirstlane_b32 s2, v210
	v_mov_b32_e32 v0, s0
	v_readfirstlane_b32 s1, v211
	v_readfirstlane_b32 s0, v8
	s_waitcnt lgkmcnt(0)
	v_readfirstlane_b32 s4, v213
	v_readfirstlane_b32 s10, v212
	s_cbranch_scc1 .LBB0_517
	v_lshlrev_b32_e32 v0, 4, v8
	v_add_u32_e32 v1, 0x2000, v0
	v_ashrrev_i32_e32 v2, 31, v1
	v_lshrrev_b32_e32 v2, 22, v2
	v_add_u32_e32 v2, v1, v2
	v_ashrrev_i32_e32 v2, 10, v2
	v_mul_i32_i24_e32 v3, 0x400, v2
	v_sub_u32_e32 v1, v1, v3
	s_add_u32 s7, s7, 0x54e1fd00
	v_lshrrev_b32_e32 v3, 4, v1
	s_addc_u32 s6, s6, 0
	s_mul_hi_i32 s12, s8, 0x60000
	s_mul_i32 s8, s8, 0x60000
	v_bitop3_b32 v1, v3, v1, 32 bitop3:0x6c
	s_add_u32 s38, s7, s8
	v_ashrrev_i32_e32 v3, 31, v1
	s_addc_u32 s39, s6, s12
	v_lshrrev_b32_e32 v3, 26, v3
	s_add_u32 s6, s11, 0x8003600
	v_add_u32_e32 v3, v1, v3
	v_lshlrev_b32_e32 v5, 3, v2
	s_addc_u32 s7, s9, 0
	v_ashrrev_i32_e32 v4, 6, v3
	v_and_b32_e32 v5, -16, v5
	s_add_u32 s48, s6, 0x1e80
	v_add_u32_e32 v5, v4, v5
	s_addc_u32 s58, s7, 0
	v_and_b32_e32 v4, 3, v4
	s_mov_b32 s7, 0x7ffffe0
	v_lshrrev_b32_e32 v6, 2, v5
	v_lshlrev_b32_e32 v7, 1, v5
	v_and_b32_e32 v3, 0xc0, v3
	v_and_or_b32 v4, v5, s7, v4
	v_and_b32_e32 v6, 4, v6
	v_and_b32_e32 v7, 24, v7
	v_lshlrev_b32_e32 v2, 5, v2
	v_sub_u32_e32 v1, v1, v3
	v_or3_b32 v4, v4, v6, v7
	s_movk_i32 s6, 0x1060
	v_and_b32_e32 v2, 32, v2
	v_ashrrev_i16_sdwa v1, v205, sext(v1) dst_sel:DWORD dst_unused:UNUSED_PAD src0_sel:DWORD src1_sel:BYTE_0
	v_mul_lo_u32 v4, v4, s6
	v_add_u32_sdwa v1, v2, sext(v1) dst_sel:DWORD dst_unused:UNUSED_PAD src0_sel:DWORD src1_sel:WORD_0
	v_lshlrev_b32_e32 v2, 9, v5
	v_add_lshl_u32 v136, v4, v1, 1
	v_lshl_add_u32 v138, v1, 1, v2
	v_bfe_i32 v1, v8, 27, 1
	v_lshrrev_b32_e32 v1, 22, v1
	v_add_u32_e32 v1, v0, v1
	v_and_b32_e32 v1, 0xfffffc00, v1
	v_sub_u32_e32 v0, v0, v1
	v_lshrrev_b32_e32 v1, 4, v0
	v_ashrrev_i32_e32 v3, 31, v8
	v_bitop3_b32 v0, v1, v0, 32 bitop3:0x6c
	v_lshrrev_b32_e32 v3, 26, v3
	v_ashrrev_i32_e32 v1, 31, v0
	v_add_u32_e32 v3, v8, v3
	v_lshrrev_b32_e32 v1, 26, v1
	v_ashrrev_i32_e32 v3, 6, v3
	v_add_u32_e32 v1, v0, v1
	v_lshlrev_b32_e32 v4, 3, v3
	v_ashrrev_i32_e32 v2, 6, v1
	v_and_b32_e32 v4, -16, v4
	v_add_u32_e32 v4, v2, v4
	v_and_b32_e32 v2, 3, v2
	v_lshrrev_b32_e32 v5, 2, v4
	v_lshlrev_b32_e32 v6, 1, v4
	v_and_or_b32 v2, v4, s7, v2
	v_and_b32_e32 v5, 4, v5
	v_and_b32_e32 v6, 24, v6
	v_or3_b32 v2, v2, v5, v6
	s_and_b32 s5, s5, 7
	v_mul_lo_u32 v2, v2, s6
	s_lshr_b32 s6, s34, 3
	s_mul_i32 s5, s5, 12
	s_add_i32 s6, s5, s6
	s_and_b32 s5, s6, 0xff
	s_mulk_i32 s5, 0xab
	s_lshr_b32 s5, s5, 9
	s_mul_i32 s7, s5, 3
	s_sub_i32 s6, s6, s7
	s_ashr_i32 s12, s0, 6
	v_and_b32_e32 v1, 0xc0, v1
	s_and_b32 s46, s6, 0xff
	s_ashr_i32 s13, s0, 8
	s_lshl_b32 s59, s12, 10
	v_lshlrev_b32_e32 v3, 5, v3
	v_sub_u32_e32 v0, v0, v1
	s_lshl_b32 s8, s46, 17
	s_mul_i32 s6, s5, 0x20c000
	v_and_b32_e32 v3, 32, v3
	v_ashrrev_i16_sdwa v0, v205, sext(v0) dst_sel:DWORD dst_unused:UNUSED_PAD src0_sel:DWORD src1_sel:BYTE_0
	s_add_u32 s22, s48, s6
	v_add_u32_sdwa v0, v3, sext(v0) dst_sel:DWORD dst_unused:UNUSED_PAD src0_sel:DWORD src1_sel:WORD_0
	s_addc_u32 s23, s58, 0
	s_add_i32 s61, s59, 0
	v_add_lshl_u32 v144, v2, v0, 1
	s_add_i32 m0, s61, 0x10000
	v_lshlrev_b32_e32 v1, 9, v4
	global_load_lds_dwordx4 v144, s[22:23]
	s_add_i32 m0, s61, 0x12000
	s_add_u32 s6, s22, 0x106000
	global_load_lds_dwordx4 v136, s[22:23]
	s_addc_u32 s7, s23, 0
	s_add_i32 m0, s61, 0x14000
	v_lshl_add_u32 v140, v0, 1, v1
	global_load_lds_dwordx4 v144, s[6:7]
	s_add_i32 m0, s61, 0x16000
	s_add_u32 s24, s38, s8
	s_addc_u32 s25, s39, 0
	s_add_i32 s68, s61, 0x2000
	global_load_lds_dwordx4 v136, s[6:7]
	s_mov_b32 m0, s61
	s_add_u32 s6, s24, 0x10000
	global_load_lds_dwordx4 v140, s[24:25]
	s_mov_b32 m0, s68
	s_addc_u32 s7, s25, 0
	s_add_i32 s69, s61, 0x4000
	global_load_lds_dwordx4 v138, s[24:25]
	s_mov_b32 m0, s69
	s_add_i32 s78, s61, 0x6000
	global_load_lds_dwordx4 v140, s[6:7]
	s_mov_b32 m0, s78
	v_mov_b32_e32 v137, v145
	global_load_lds_dwordx4 v138, s[6:7]
	v_mov_b32_e32 v141, v145
	v_mov_b32_e32 v139, v145
	s_cmp_eq_u32 s13, 1
	v_lshl_add_u64 v[6:7], s[22:23], 0, v[144:145]
	v_lshl_add_u64 v[4:5], s[22:23], 0, v[136:137]
	v_lshl_add_u64 v[0:1], s[24:25], 0, v[140:141]
	s_cselect_b64 s[6:7], -1, 0
	s_cmp_lg_u32 s13, 1
	v_lshl_add_u64 v[2:3], s[24:25], 0, v[138:139]
	s_cbranch_scc1 .LBB0_491
	s_barrier

.LBB0_517:
	s_mov_b32 s0, s37
	s_mov_b32 s1, s33
	v_mbcnt_lo_u32_b32 v0, -1, s0
	v_mbcnt_hi_u32_b32 v0, -1, v0
	v_lshl_or_b32 v0, s1, 6, v0
	v_readlane_b32 s0, v254, 0
	v_readlane_b32 s1, v254, 1
	s_mov_b32 s1, s0
	s_mov_b32 s0, s37
	s_add_i32 s0, s0, 0x20120
	v_mov_b32_e32 v1, s0
	v_mov_b32_e32 v251, 0x20000
	ds_read_b64 v[206:207], v251 offset:288
	ds_read_b64 v[208:209], v251 offset:64
	ds_read_b64 v[210:211], v251 offset:72
	ds_read_b64 v[212:213], v251 offset:80
	ds_read_b64 v[214:215], v251 offset:88
	ds_read_b64 v[216:217], v251 offset:96
	ds_read_b64 v[218:219], v251 offset:104
	ds_read_b64 v[224:225], v251 offset:112
	ds_read_b64 v[226:227], v251 offset:120
	ds_read_b64 v[228:229], v251 offset:288
	ds_read_b64 v[230:231], v251 offset:288
	ds_read_b64 v[232:233], v251 offset:288
	s_mov_b32 s4, 0
	s_add_i32 s4, s4, 0x20040
	v_mov_b32_e32 v1, s4
	s_waitcnt lgkmcnt(0)
	v_readfirstlane_b32 s0, v207
	v_readfirstlane_b32 s2, v206
	s_mov_b32 s6, s60
	s_mov_b32 s7, 0
	s_add_i32 s7, s7, 0x20048
	v_mov_b32_e32 v1, s7
	s_waitcnt lgkmcnt(0)
	v_readfirstlane_b32 s4, v209
	v_readfirstlane_b32 s5, v208
	s_mov_b32 s15, s60
	s_mov_b32 s8, 0
	s_add_i32 s8, s8, 0x20050
	v_mov_b32_e32 v1, s8
	s_waitcnt lgkmcnt(0)
	v_readfirstlane_b32 s7, v211
	v_readfirstlane_b32 s14, v210
	s_mov_b32 s18, s60
	s_mov_b32 s8, 0
	s_add_i32 s8, s8, 0x20058
	v_mov_b32_e32 v1, s8
	s_waitcnt lgkmcnt(0)
	v_readfirstlane_b32 s17, v213
	v_readfirstlane_b32 s16, v212
	s_mov_b32 s21, s60
	s_mov_b32 s8, 0
	s_add_i32 s8, s8, 0x20060
	v_mov_b32_e32 v1, s8
	s_waitcnt lgkmcnt(0)
	v_readfirstlane_b32 s19, v215
	v_readfirstlane_b32 s20, v214
	s_mov_b32 s24, s60
	s_mov_b32 s8, 0
	s_add_i32 s8, s8, 0x20068
	v_mov_b32_e32 v1, s8
	s_waitcnt lgkmcnt(0)
	v_readfirstlane_b32 s22, v217
	v_readfirstlane_b32 s23, v216
	s_mov_b32 s28, s60
	s_mov_b32 s8, 0
	s_add_i32 s8, s8, 0x20070
	v_mov_b32_e32 v1, s8
	s_waitcnt lgkmcnt(0)
	v_readfirstlane_b32 s26, v219
	v_readfirstlane_b32 s27, v218
	s_mov_b32 s31, s60
	s_mov_b32 s8, 0
	s_add_i32 s8, s8, 0x20078
	v_mov_b32_e32 v1, s8
	s_waitcnt lgkmcnt(0)
	v_readfirstlane_b32 s29, v225
	v_readfirstlane_b32 s30, v224
	s_mov_b32 s35, s60
	s_mov_b32 s8, 0
	s_add_i32 s8, s8, 0x20120
	v_mov_b32_e32 v1, s8
	s_waitcnt lgkmcnt(0)
	v_readfirstlane_b32 s25, v227
	v_readfirstlane_b32 s34, v226
	s_mov_b32 s8, 0
	s_add_i32 s8, s8, 0x20120
	v_mov_b32_e32 v1, s8
	s_waitcnt lgkmcnt(0)
	v_readfirstlane_b32 s36, v229
	v_readfirstlane_b32 s39, v228
	s_mov_b32 s8, 0
	s_add_i32 s8, s8, 0x20120
	v_mov_b32_e32 v1, s8
	s_waitcnt lgkmcnt(0)
	v_readfirstlane_b32 s38, v231
	v_readfirstlane_b32 s44, v230
	v_ashrrev_i32_e32 v1, 6, v0
	v_lshl_add_u32 v90, s1, 3, v1
	s_movk_i32 s1, 0xe00
	v_cmp_gt_i32_e32 vcc, s1, v90
	s_waitcnt lgkmcnt(0)
	v_readfirstlane_b32 s45, v233
	v_readfirstlane_b32 s46, v232
	s_and_saveexec_b64 s[8:9], vcc
	s_cbranch_execz .LBB0_536
	s_add_u32 s10, s2, 0x8003600
	s_addc_u32 s11, s0, 0
	s_mul_hi_i32 s0, s6, 0x1c00
	s_mulk_i32 s6, 0x1c00
	s_add_u32 s12, s5, s6
	s_addc_u32 s13, s4, s0
	s_mul_hi_i32 s0, s15, 0x1c00
	s_mulk_i32 s15, 0x1c00
	s_add_u32 s14, s14, s15
	s_addc_u32 s15, s7, s0
	s_mul_hi_i32 s0, s18, 0x70
	s_mulk_i32 s18, 0x70
	s_add_u32 s16, s16, s18
	s_addc_u32 s17, s17, s0
	s_mul_hi_i32 s0, s21, 0x1c000
	s_mul_i32 s21, s21, 0x1c000
	s_add_u32 s18, s20, s21
	s_addc_u32 s19, s19, s0
	s_mul_hi_i32 s0, s24, 0x1c000
	s_mul_i32 s24, s24, 0x1c000
	s_add_u32 s20, s23, s24
	s_addc_u32 s21, s22, s0
	s_mul_hi_i32 s0, s35, 0x700
	s_mulk_i32 s35, 0x700
	s_add_u32 s22, s34, s35
	s_addc_u32 s23, s25, s0
	s_add_u32 s24, s39, 0x1944b600
	s_movk_i32 s0, 0x2100
	s_addc_u32 s25, s36, 0
	v_mul_lo_u32 v2, v1, s0
	v_lshlrev_b32_e32 v1, 11, v1
	v_readlane_b32 s0, v254, 7
	s_mul_hi_i32 s2, s31, 0x1c000
	s_mul_i32 s31, s31, 0x1c000
	v_add_u32_e32 v5, s0, v1
	s_add_u32 s0, s46, 0x4f59fd00
	s_addc_u32 s1, s45, 0
	s_add_u32 s4, s44, 0x197cb600
	s_addc_u32 s5, s38, 0
	s_add_u32 s6, s30, s31
	s_addc_u32 s2, s29, s2
	s_mul_hi_i32 s7, s28, 0x1c000
	s_mul_i32 s28, s28, 0x1c000
	s_add_u32 s27, s27, s28
	v_and_b32_e32 v91, 63, v0
	s_addc_u32 s7, s26, s7
	v_add_u32_e32 v4, 0, v2
	v_mov_b32_e32 v2, s2
	v_mov_b32_e32 v3, s7
	v_cmp_gt_u32_e32 vcc, 32, v91
	v_and_b32_e32 v92, 15, v0
	v_bfe_u32 v6, v0, 4, 2
	v_cndmask_b32_e32 v3, v2, v3, vcc
	v_mov_b32_e32 v2, s6
	v_mov_b32_e32 v7, s27
	v_lshlrev_b32_e32 v0, 3, v0
	v_cndmask_b32_e32 v2, v2, v7, vcc
	v_and_b32_e32 v144, 0x80, v0
	v_lshl_add_u64 v[64:65], v[2:3], 0, v[144:145]
	v_mul_u32_u24_e32 v0, 0x1060, v91
	v_lshlrev_b32_e32 v7, 5, v91
	v_lshl_add_u32 v94, v91, 2, v4
	v_lshl_add_u32 v4, v6, 7, v4
	v_mul_u32_u24_e32 v8, 0x210, v92
	v_lshlrev_b32_e32 v2, 1, v92
	v_lshlrev_b32_e32 v144, 2, v92
	v_mov_b32_e32 v3, v145
	v_cndmask_b32_e64 v93, -1.0, 1.0, vcc
	v_lshlrev_b32_e32 v95, 2, v6
	v_add_u32_e32 v96, v5, v2
	v_lshl_add_u64 v[66:67], s[4:5], 0, v[144:145]
	v_lshl_add_u64 v[68:69], s[0:1], 0, v[2:3]
	v_add_u32_e32 v97, 0, v1
	s_mov_b64 s[26:27], 0
	v_lshlrev_b32_e32 v70, 1, v0
	v_add_u32_e32 v98, v5, v7
	v_add_u32_e32 v99, v4, v8

.LBB0_580:
	s_or_b64 exec, exec, s[64:65]
	s_mov_b32 s0, s37
	s_waitcnt lgkmcnt(0)
	s_barrier
	s_mov_b32 s1, s33
	v_mbcnt_lo_u32_b32 v0, -1, s0
	v_mbcnt_hi_u32_b32 v0, -1, v0
	v_lshl_or_b32 v8, s1, 6, v0
	v_readlane_b32 s0, v254, 0
	s_mov_b32 s8, s0
	s_cmpk_lt_i32 s8, 0xc0
	s_mov_b32 s20, 0x38e38e39
	s_mov_b32 s21, 0xe38e38e
	v_readlane_b32 s1, v254, 1
	s_cbranch_scc1 .LBB0_653
	s_mov_b32 s0, s37
	s_add_i32 s0, s0, 0x20120
	v_mov_b32_e32 v0, s0
	v_mov_b32_e32 v251, 0x20000
	ds_read_b64 v[206:207], v251 offset:288
	ds_read_b64 v[208:209], v251 offset:288
	ds_read_b64 v[210:211], v251 offset:288
	ds_read_b64 v[212:213], v251 offset:136
	ds_read_b64 v[214:215], v251 offset:288
	s_mov_b32 s0, 0
	s_add_i32 s0, s0, 0x20120
	s_mov_b32 s7, 0
	s_waitcnt lgkmcnt(0)
	v_readfirstlane_b32 s4, v206
	v_mov_b32_e32 v0, s0
	v_readfirstlane_b32 s2, v207
	s_mov_b32 s0, s60
	s_add_i32 s7, s7, 0x20120
	s_waitcnt lgkmcnt(0)
	v_readfirstlane_b32 s6, v208
	v_mov_b32_e32 v0, s7
	v_readfirstlane_b32 s1, v209
	s_mov_b32 s7, 0
	s_add_i32 s7, s7, 0x20088
	s_mov_b32 s16, s60
	s_waitcnt lgkmcnt(0)
	v_readfirstlane_b32 s13, v210
	v_mov_b32_e32 v0, s7
	v_readfirstlane_b32 s12, v211
	s_mov_b32 s7, 0
	s_add_i32 s7, s7, 0x20120
	s_waitcnt lgkmcnt(0)
	v_readfirstlane_b32 s15, v212
	v_mov_b32_e32 v0, s7
	v_readfirstlane_b32 s14, v213
	s_add_i32 s5, s8, 0xffffff40
	v_readfirstlane_b32 s19, v8
	s_cmp_gt_u32 s5, 63
	s_waitcnt lgkmcnt(0)
	v_readfirstlane_b32 s17, v215
	v_readfirstlane_b32 s18, v214
	s_cbranch_scc1 .LBB0_653
	v_lshlrev_b32_e32 v0, 4, v8
	v_add_u32_e32 v1, 0x2000, v0
	v_ashrrev_i32_e32 v2, 31, v1
	v_lshrrev_b32_e32 v2, 22, v2
	v_add_u32_e32 v2, v1, v2
	v_ashrrev_i32_e32 v9, 10, v2
	v_mul_i32_i24_e32 v3, 0x400, v9
	v_sub_u32_e32 v1, v1, v3
	v_lshrrev_b32_e32 v3, 4, v1
	v_bitop3_b32 v1, v3, v1, 32 bitop3:0x6c
	v_ashrrev_i32_e32 v3, 31, v1
	v_lshrrev_b32_e32 v3, 26, v3
	v_add_u32_e32 v3, v1, v3
	v_ashrrev_i32_e32 v11, 6, v3
	v_and_b32_e32 v3, 0xc0, v3
	v_sub_u32_e32 v1, v1, v3
	v_lshlrev_b32_e32 v2, 5, v9
	v_ashrrev_i16_sdwa v1, v205, sext(v1) dst_sel:DWORD dst_unused:UNUSED_PAD src0_sel:DWORD src1_sel:BYTE_0
	v_and_b32_e32 v2, 32, v2
	v_bfe_i32 v12, v1, 0, 16
	v_add_u32_e32 v1, v2, v12
	v_lshlrev_b32_e32 v2, 3, v9
	v_and_b32_e32 v2, 0x3ffff0, v2
	v_add_lshl_u32 v2, v11, v2, 10
	v_lshl_add_u32 v128, v1, 1, v2
	v_bfe_i32 v2, v8, 27, 1
	v_lshrrev_b32_e32 v2, 22, v2
	v_add_u32_e32 v2, v0, v2
	s_ashr_i32 s9, s19, 6
	v_and_b32_e32 v2, 0xfffffc00, v2
	s_ashr_i32 s10, s19, 8
	s_lshl_b32 s20, s9, 10
	v_sub_u32_e32 v0, v0, v2
	v_lshrrev_b32_e32 v2, 4, v0
	s_add_u32 s29, s6, 0x54c5fd00
	v_bitop3_b32 v0, v2, v0, 32 bitop3:0x6c
	s_addc_u32 s30, s1, 0
	s_ashr_i32 s1, s0, 31
	v_ashrrev_i32_e32 v2, 31, v0
	s_lshl_b64 s[6:7], s[0:1], 19
	v_ashrrev_i32_e32 v1, 31, v8
	v_lshrrev_b32_e32 v2, 26, v2
	s_add_u32 s0, s29, s6
	v_lshrrev_b32_e32 v1, 26, v1
	v_add_u32_e32 v2, v0, v2
	s_addc_u32 s1, s30, s7
	v_add_u32_e32 v1, v8, v1
	v_ashrrev_i32_e32 v13, 6, v2
	v_and_b32_e32 v2, 0xc0, v2
	s_add_u32 s11, s4, 0x4f59fd00
	v_ashrrev_i32_e32 v10, 6, v1
	v_sub_u32_e32 v0, v0, v2
	s_addc_u32 s2, s2, 0
	s_lshl_b32 s4, s8, 2
	v_lshlrev_b32_e32 v1, 5, v10
	v_ashrrev_i16_sdwa v0, v205, sext(v0) dst_sel:DWORD dst_unused:UNUSED_PAD src0_sel:DWORD src1_sel:BYTE_0
	s_lshr_b32 s31, s5, 3
	s_and_b32 s4, s4, 24
	v_and_b32_e32 v1, 32, v1
	v_bfe_i32 v14, v0, 0, 16
	s_and_b32 s21, s8, 1
	s_or_b32 s22, s4, s31
	v_add_u32_e32 v0, v1, v14
	v_lshlrev_b32_e32 v1, 3, v10
	s_lshl_b32 s24, s22, 18
	s_lshl_b32 s34, s21, 18
	v_and_b32_e32 v1, 0x3ffff0, v1
	s_add_u32 s0, s0, s34
	v_add_lshl_u32 v1, v13, v1, 10
	s_addc_u32 s1, s1, 0
	s_add_i32 s23, s20, 0
	v_lshl_add_u32 v144, v0, 1, v1
	s_add_i32 m0, s23, 0x10000
	v_mov_b32_e32 v129, v145
	global_load_lds_dwordx4 v144, s[0:1]
	s_add_i32 m0, s23, 0x12000
	s_add_u32 s4, s0, 0x20000
	global_load_lds_dwordx4 v128, s[0:1]
	s_addc_u32 s5, s1, 0
	s_add_i32 m0, s23, 0x14000
	v_lshl_add_u64 v[6:7], s[0:1], 0, v[144:145]
	global_load_lds_dwordx4 v144, s[4:5]
	s_add_i32 m0, s23, 0x16000
	v_lshl_add_u64 v[4:5], s[0:1], 0, v[128:129]
	global_load_lds_dwordx4 v128, s[4:5]
	s_add_u32 s4, s11, s24
	s_addc_u32 s5, s2, 0
	s_add_i32 s24, s23, 0x2000
	s_mov_b32 m0, s23
	s_add_u32 s38, s4, 0x20000
	global_load_lds_dwordx4 v144, s[4:5]
	s_mov_b32 m0, s24
	s_addc_u32 s39, s5, 0
	s_add_i32 s25, s23, 0x4000
	global_load_lds_dwordx4 v128, s[4:5]
	s_mov_b32 m0, s25
	s_add_i32 s26, s23, 0x6000
	global_load_lds_dwordx4 v144, s[38:39]
	s_mov_b32 m0, s26
	v_lshl_add_u64 v[2:3], s[4:5], 0, v[144:145]
	global_load_lds_dwordx4 v128, s[38:39]
	s_cmp_lg_u32 s10, 1
	v_lshl_add_u64 v[0:1], s[4:5], 0, v[128:129]
	s_cbranch_scc1 .LBB0_584
	s_barrier

.LBB0_653:
	s_mov_b32 s0, s37
	s_mov_b32 s1, s33
	v_mbcnt_lo_u32_b32 v0, -1, s0
	v_mbcnt_hi_u32_b32 v0, -1, v0
	v_lshl_or_b32 v0, s1, 6, v0
	v_readlane_b32 s0, v254, 0
	v_readlane_b32 s1, v254, 1
	s_mov_b32 s1, s37
	s_add_i32 s1, s1, 0x20120
	v_mov_b32_e32 v1, s1
	v_mov_b32_e32 v251, 0x20000
	ds_read_b64 v[206:207], v251 offset:288
	ds_read_b64 v[208:209], v251 offset:288
	ds_read_b64 v[210:211], v251 offset:288
	s_mov_b32 s1, 0
	s_add_i32 s1, s1, 0x20120
	v_mov_b32_e32 v1, s1
	s_waitcnt lgkmcnt(0)
	v_readfirstlane_b32 s2, v207
	v_readfirstlane_b32 s4, v206
	s_mov_b32 s1, 0
	s_add_i32 s1, s1, 0x20120
	v_mov_b32_e32 v1, s1
	s_waitcnt lgkmcnt(0)
	v_readfirstlane_b32 s7, v209
	v_readfirstlane_b32 s6, v208
	s_ashr_i32 s1, s0, 31
	s_lshl_b64 s[0:1], s[0:1], 9
	v_ashrrev_i32_e32 v1, 31, v0
	v_lshl_add_u64 v[0:1], s[0:1], 0, v[0:1]
	s_mov_b64 s[0:1], 0x90000
	s_waitcnt lgkmcnt(0)
	v_readfirstlane_b32 s9, v211
	v_readfirstlane_b32 s8, v210
	v_cmp_gt_i64_e32 vcc, s[0:1], v[0:1]
	s_and_saveexec_b64 s[0:1], vcc
	s_cbranch_execz .LBB0_656
	s_add_u32 s4, s4, 0x18203600
	s_addc_u32 s5, s2, 0
	s_add_u32 s6, s6, 0x19403600
	s_addc_u32 s7, s7, 0
	s_add_u32 s8, s8, 0x4cb9fd00
	s_addc_u32 s9, s9, 0
	v_lshlrev_b32_e32 v2, 3, v0
	s_mov_b64 s[10:11], 0

.LBB0_656:
	s_or_b64 exec, exec, s[0:1]
	s_mov_b32 s0, 0
	s_mov_b32 s1, s33
	v_mbcnt_lo_u32_b32 v0, -1, s0
	v_mbcnt_hi_u32_b32 v0, -1, v0
	v_lshl_or_b32 v0, s1, 6, v0
	v_readlane_b32 s0, v254, 0
	s_mov_b32 s28, s0
	s_mov_b32 s0, s37
	s_add_i32 s0, s0, 0x20120
	v_mov_b32_e32 v1, s0
	v_mov_b32_e32 v251, 0x20000
	ds_read_b64 v[206:207], v251 offset:288
	ds_read_b64 v[208:209], v251 offset:288
	ds_read_b64 v[210:211], v251 offset:288
	ds_read_b64 v[212:213], v251 offset:288
	ds_read_b64 v[214:215], v251 offset:288
	ds_read_b64 v[216:217], v251 offset:288
	ds_read_b64 v[218:219], v251 offset:288
	v_readlane_b32 s1, v254, 1
	s_mov_b32 s2, 0
	v_bfe_u32 v8, v0, 6, 2
	s_waitcnt lgkmcnt(0)
	v_readfirstlane_b32 s0, v206
	v_readfirstlane_b32 s1, v207
	s_add_u32 s0, s0, 0x54edfd00
	s_addc_u32 s1, s1, 0
	s_add_i32 s2, s2, 0x20120
	v_mov_b32_e32 v1, s2
	v_and_b32_e32 v144, 48, v0
	v_ashrrev_i32_e32 v7, 8, v0
	v_lshl_add_u64 v[142:143], s[0:1], 0, v[144:145]
	v_bfe_u32 v4, v0, 4, 2
	s_waitcnt lgkmcnt(0)
	v_readfirstlane_b32 s4, v208
	v_readfirstlane_b32 s2, v209
	s_add_u32 s29, s4, 0x55c5fd00
	s_addc_u32 s30, s2, 0
	s_mov_b32 s2, 0
	s_add_i32 s2, s2, 0x20120
	v_mov_b32_e32 v1, s2
	v_lshlrev_b32_e32 v5, 3, v4
	v_lshlrev_b32_e32 v164, 2, v4
	v_add_u32_e32 v4, 0x200, v0
	v_lshrrev_b32_e32 v6, 6, v0
	s_waitcnt lgkmcnt(0)
	v_readfirstlane_b32 s4, v210
	v_readfirstlane_b32 s2, v211
	s_add_u32 s14, s4, 0x8003600
	s_addc_u32 s15, s2, 0
	s_mov_b32 s2, 0
	s_add_i32 s2, s2, 0x20120
	v_mov_b32_e32 v1, s2
	v_and_b32_e32 v140, 15, v0
	v_ashrrev_i32_e32 v224, 4, v0
	s_mov_b32 s31, 0
	v_mov_b32_e32 v171, v145
	s_waitcnt lgkmcnt(0)
	v_readfirstlane_b32 s4, v212
	v_readfirstlane_b32 s2, v213
	s_add_u32 s4, s4, 0x565dfd00
	s_addc_u32 s5, s2, 0
	s_mov_b32 s2, 0
	s_add_i32 s2, s2, 0x20120
	v_mov_b32_e32 v1, s2
	v_mov_b32_e32 v177, v145
	v_mov_b32_e32 v183, v145
	v_mul_u32_u24_e32 v235, 0xd0, v140
	v_mul_u32_u24_e32 v236, 0x110, v140
	s_waitcnt lgkmcnt(0)
	v_readfirstlane_b32 s6, v214
	v_readfirstlane_b32 s2, v215
	s_add_u32 s16, s6, 0x4cb9fd00
	s_addc_u32 s17, s2, 0
	s_mov_b32 s2, 0
	s_add_i32 s2, s2, 0x20120
	v_mov_b32_e32 v1, s2
	v_lshl_or_b32 v238, v7, 6, 63
	s_waitcnt lgkmcnt(0)
	v_readfirstlane_b32 s6, v216
	v_readfirstlane_b32 s2, v217
	s_add_u32 s6, s6, 0x1a64b600
	s_addc_u32 s7, s2, 0
	s_mov_b32 s2, 0
	s_add_i32 s2, s2, 0x20120
	v_mov_b32_e32 v1, s2
	v_and_b32_e32 v1, 63, v0
	v_lshlrev_b32_e32 v9, 2, v1
	v_cmp_gt_u32_e64 s[0:1], 32, v1
	v_lshlrev_b32_e32 v1, 3, v0
	s_waitcnt lgkmcnt(0)
	v_readfirstlane_b32 s8, v218
	v_readfirstlane_b32 s2, v219
	s_add_u32 s8, s8, 0x1a6cb600
	v_mov_b32_e32 v2, 0x780
	s_addc_u32 s9, s2, 0
	v_lshl_or_b32 v141, v8, 5, v2
	v_lshlrev_b32_e32 v2, 1, v0
	s_movk_i32 s2, 0x3400
	v_and_b32_e32 v2, 32, v2
	v_mov_b32_e32 v3, v145
	v_and_b32_e32 v10, 0x78, v1
	v_mad_i32_i24 v1, v7, s2, 0
	v_readlane_b32 s2, v254, 8
	v_xor_b32_e32 v165, 0x80, v9
	v_lshl_add_u64 v[158:159], s[6:7], 0, v[2:3]
	v_lshl_add_u64 v[160:161], s[8:9], 0, v[2:3]
	v_lshlrev_b32_e32 v2, 1, v10
	v_xor_b32_e32 v227, 64, v9
	v_add_u32_e32 v9, s2, v9
	s_movk_i32 s2, 0x100
	v_lshl_add_u64 v[162:163], s[4:5], 0, v[2:3]
	v_mul_i32_i24_e32 v2, 0xffffcc80, v7
	v_cmp_gt_u32_e64 s[6:7], s2, v0
	s_mov_b32 s2, 0x2aaaaaab
	v_add_u32_e32 v225, v1, v144
	v_add3_u32 v226, v1, v2, v5
	v_mul_hi_i32 v1, v0, s2
	v_lshrrev_b32_e32 v2, 31, v1
	v_ashrrev_i32_e32 v1, 1, v1
	v_add_u32_e32 v166, v1, v2
	v_mad_u64_u32 v[2:3], s[8:9], v166, -12, v[0:1]
	v_mul_hi_i32 v1, v4, s2
	v_lshrrev_b32_e32 v3, 31, v1
	v_ashrrev_i32_e32 v1, 1, v1
	v_add_u32_e32 v0, 0x400, v0
	v_add_u32_e32 v172, v1, v3
	v_mul_hi_i32 v1, v0, s2
	v_lshrrev_b32_e32 v3, 31, v1
	v_ashrrev_i32_e32 v1, 1, v1
	v_add_u32_e32 v178, v1, v3
	s_movk_i32 s2, 0xd0
	v_mul_lo_u32 v229, v166, s2
	v_mul_lo_u32 v231, v172, s2
	v_mul_lo_u32 v233, v178, s2
	s_movk_i32 s2, 0x88
	v_mul_lo_u32 v3, v224, s2
	v_mad_u64_u32 v[4:5], s[10:11], v172, -12, v[4:5]
	v_mad_u64_u32 v[0:1], s[12:13], v178, -12, v[0:1]
	v_add_lshl_u32 v234, v3, v10, 1
	s_movk_i32 s2, 0x110
	v_mov_b32_e32 v3, 0x1100
	v_lshlrev_b32_e32 v228, 4, v2
	v_lshlrev_b32_e32 v230, 4, v4
	v_lshlrev_b32_e32 v232, 4, v0
	v_mad_u32_u24 v237, v140, s2, v3
	s_movk_i32 s2, 0x2400
	v_cmp_lt_i32_e64 s[8:9], 7, v2
	v_lshlrev_b32_e32 v168, 3, v2
	v_cmp_lt_i32_e64 s[10:11], 7, v4
	v_lshlrev_b32_e32 v174, 3, v4
	v_cmp_lt_i32_e64 s[12:13], 7, v0
	v_lshlrev_b32_e32 v180, 3, v0
	v_add_u32_e32 v1, 0, v228
	v_add_u32_e32 v2, 0, v230
	v_add_u32_e32 v0, 0, v232
	v_mul_u32_u24_e32 v3, 0x2400, v8
	v_mul_lo_u32 v4, v6, s2
	s_sub_i32 s34, 0xff, s28
	v_cmp_eq_u32_e64 s[4:5], 1, v7
	v_ashrrev_i32_e32 v167, 31, v166
	v_subrev_u32_e32 v170, 64, v168
	v_ashrrev_i32_e32 v169, 31, v168
	v_ashrrev_i32_e32 v173, 31, v172
	v_subrev_u32_e32 v176, 64, v174
	v_ashrrev_i32_e32 v175, 31, v174
	v_ashrrev_i32_e32 v179, 31, v178
	v_subrev_u32_e32 v182, 64, v180
	v_ashrrev_i32_e32 v181, 31, v180
	v_add_u32_e32 v239, v1, v229
	v_add_u32_e32 v240, v2, v231
	v_add_u32_e32 v241, v0, v233
	v_add_u32_e32 v242, v9, v3
	v_add_u32_e32 v243, v9, v4
	s_branch .LBB0_659

.LBB0_743:
	s_or_b64 exec, exec, s[64:65]
	s_mov_b32 s0, s37
	s_waitcnt lgkmcnt(0)
	s_barrier
	s_mov_b32 s1, s33
	v_mbcnt_lo_u32_b32 v0, -1, s0
	v_mbcnt_hi_u32_b32 v0, -1, v0
	v_lshl_or_b32 v8, s1, 6, v0
	v_readlane_b32 s0, v254, 0
	s_mov_b32 s28, s0
	s_mov_b32 s0, s37
	s_add_i32 s0, s0, 0x20120
	v_mov_b32_e32 v0, s0
	v_mov_b32_e32 v251, 0x20000
	ds_read_b64 v[206:207], v251 offset:288
	ds_read_b64 v[208:209], v251 offset:288
	ds_read_b64 v[210:211], v251 offset:288
	s_mov_b32 s0, 0
	s_add_i32 s0, s0, 0x20120
	v_readlane_b32 s1, v254, 1
	s_waitcnt lgkmcnt(0)
	v_readfirstlane_b32 s7, v206
	v_mov_b32_e32 v0, s0
	v_readfirstlane_b32 s1, v207
	s_mov_b32 s0, s60
	s_mov_b32 s2, 0
	s_add_i32 s2, s2, 0x20120
	s_waitcnt lgkmcnt(0)
	v_readfirstlane_b32 s11, v208
	v_mov_b32_e32 v0, s2
	v_readfirstlane_b32 s10, v209
	s_cmpk_lt_i32 s28, 0x100
	v_readfirstlane_b32 s14, v8
	s_cselect_b64 s[8:9], -1, 0
	s_cmpk_gt_i32 s28, 0xff
	s_waitcnt lgkmcnt(0)
	v_readfirstlane_b32 s2, v211
	v_readfirstlane_b32 s12, v210
	s_cbranch_scc1 .LBB0_749
	s_ashr_i32 s4, s28, 31
	s_lshr_b32 s4, s4, 29
	s_add_i32 s6, s28, s4
	s_and_b32 s4, s6, -8
	s_sub_i32 s13, s28, s4
	s_cmp_gt_i32 s13, -1
	s_mov_b64 s[4:5], -1
	s_cbranch_scc0 .LBB0_746
	s_lshl_b32 s15, s13, 5
	s_mov_b64 s[4:5], 0

.LBB0_940:
	s_or_b64 exec, exec, s[64:65]
	s_mov_b32 s0, s37
	s_waitcnt lgkmcnt(0)
	s_barrier
	s_mov_b32 s1, s33
	v_mbcnt_lo_u32_b32 v0, -1, s0
	v_mbcnt_hi_u32_b32 v0, -1, v0
	v_lshl_or_b32 v2, s1, 6, v0
	v_readlane_b32 s0, v254, 0
	s_mov_b32 s17, s0
	s_mov_b32 s0, s37
	s_add_i32 s0, s0, 0x20120
	v_mov_b32_e32 v0, s0
	v_mov_b32_e32 v251, 0x20000
	ds_read_b64 v[206:207], v251 offset:288
	ds_read_b64 v[208:209], v251 offset:288
	ds_read_b64 v[210:211], v251 offset:288
	ds_read_b64 v[212:213], v251 offset:288
	ds_read_b64 v[214:215], v251 offset:288
	ds_read_b64 v[216:217], v251 offset:288
	ds_read_b64 v[218:219], v251 offset:184
	ds_read_b64 v[224:225], v251 offset:288
	ds_read_b64 v[226:227], v251 offset:288
	ds_read_b64 v[228:229], v251 offset:288
	s_mov_b32 s0, 0
	s_add_i32 s0, s0, 0x20120
	s_mov_b32 s4, s60
	s_waitcnt lgkmcnt(0)
	v_readfirstlane_b32 s16, v206
	v_mov_b32_e32 v0, s0
	v_readfirstlane_b32 s14, v207
	s_mov_b32 s0, 0
	s_add_i32 s0, s0, 0x20120
	v_readlane_b32 s1, v254, 1
	s_waitcnt lgkmcnt(0)
	v_readfirstlane_b32 s12, v208
	v_mov_b32_e32 v0, s0
	v_readfirstlane_b32 s5, v209
	s_mov_b32 s0, 0
	s_add_i32 s0, s0, 0x20120
	s_waitcnt lgkmcnt(0)
	v_readfirstlane_b32 s8, v210
	v_mov_b32_e32 v0, s0
	v_readfirstlane_b32 s2, v211
	s_mov_b32 s0, 0
	s_add_i32 s0, s0, 0x20120
	s_waitcnt lgkmcnt(0)
	v_readfirstlane_b32 s23, v212
	v_mov_b32_e32 v0, s0
	v_readfirstlane_b32 s22, v213
	s_mov_b32 s0, 0
	s_add_i32 s0, s0, 0x20120
	s_waitcnt lgkmcnt(0)
	v_readfirstlane_b32 s15, v214
	v_mov_b32_e32 v0, s0
	v_readfirstlane_b32 s13, v215
	s_mov_b32 s0, 0
	s_add_i32 s0, s0, 0x200b8
	s_waitcnt lgkmcnt(0)
	v_readfirstlane_b32 s19, v216
	v_mov_b32_e32 v0, s0
	v_readfirstlane_b32 s18, v217
	s_mov_b32 s0, 0
	s_add_i32 s0, s0, 0x20120
	s_waitcnt lgkmcnt(0)
	v_readfirstlane_b32 s25, v218
	v_mov_b32_e32 v0, s0
	v_readfirstlane_b32 s24, v219
	s_mov_b32 s0, 0
	s_add_i32 s0, s0, 0x20120
	s_waitcnt lgkmcnt(0)
	v_readfirstlane_b32 s21, v224
	v_mov_b32_e32 v0, s0
	v_readfirstlane_b32 s20, v225
	s_mov_b32 s0, 0
	s_add_i32 s0, s0, 0x20120
	s_waitcnt lgkmcnt(0)
	v_readfirstlane_b32 s27, v226
	v_mov_b32_e32 v0, s0
	v_readfirstlane_b32 s26, v227
	v_cmp_eq_u32_e64 s[0:1], 0, v2
	s_waitcnt lgkmcnt(0)
	v_readfirstlane_b32 s28, v229
	v_readfirstlane_b32 s29, v228
	s_and_saveexec_b64 s[6:7], s[0:1]
	s_cbranch_execz .LBB0_942
	v_readlane_b32 s9, v254, 9
	v_mov_b32_e32 v1, s2
	s_nop 0
	v_mov_b32_e32 v0, s9
	ds_write_b32 v0, v145
	v_mov_b32_e32 v0, s8
	v_add_co_u32_e32 v0, vcc, 0x1e76b000, v0
	s_add_u32 s8, s8, 0x1e76b600
	s_nop 0
	v_addc_co_u32_e32 v1, vcc, 0, v1, vcc
	global_load_dwordx4 v[68:71], v[0:1], off offset:1536
	global_load_dwordx4 v[72:75], v[0:1], off offset:1552
	global_load_dwordx4 v[76:79], v[0:1], off offset:1568
	global_load_dwordx4 v[80:83], v[0:1], off offset:1584
	global_load_dwordx4 v[84:87], v[0:1], off offset:1600
	global_load_dwordx4 v[88:91], v[0:1], off offset:1616
	global_load_dwordx4 v[92:95], v[0:1], off offset:1632
	global_load_dwordx4 v[96:99], v[0:1], off offset:1648
	global_load_dwordx4 v[100:103], v[0:1], off offset:1664
	global_load_dwordx4 v[104:107], v[0:1], off offset:1680
	global_load_dwordx4 v[108:111], v[0:1], off offset:1696
	global_load_dwordx4 v[112:115], v[0:1], off offset:1712
	global_load_dwordx4 v[116:119], v[0:1], off offset:1728
	global_load_dwordx4 v[120:123], v[0:1], off offset:1744
	global_load_dwordx4 v[124:127], v[0:1], off offset:1760
	global_load_dwordx4 v[128:131], v[0:1], off offset:1776
	s_waitcnt vmcnt(0)
	v_mov_b32_e32 v3, v68
	v_readlane_b32 s9, v254, 10
	s_nop 0
	v_add_u32_e32 v3, 0x13f, v3
	v_mov_b32_e32 v4, s9
	s_addc_u32 s9, s2, 0
	v_mov_b64_e32 v[0:1], s[8:9]
	s_mov_b32 s8, 0x66666667
	v_mul_hi_i32 v3, v3, s8
	v_lshrrev_b32_e32 v5, 31, v3
	v_ashrrev_i32_e32 v3, 7, v3
	v_add_u32_e32 v3, v3, v5
	s_movk_i32 s2, 0x140
	v_mul_lo_u32 v3, v3, s2
	ds_write_b32 v4, v3
	v_mov_b32_e32 v4, v69
	v_readlane_b32 s9, v254, 11
	s_nop 0
	v_add_u32_e32 v4, 0x13f, v4
	v_mul_hi_i32 v6, v4, s8
	v_lshrrev_b32_e32 v7, 31, v6
	v_ashrrev_i32_e32 v6, 7, v6
	v_add_u32_e32 v6, v6, v7
	v_mul_lo_u32 v6, v6, s2
	v_sub_u32_e32 v6, v6, v4
	v_mov_b32_e32 v5, s9
	v_add3_u32 v3, v4, v3, v6
	ds_write_b32 v5, v3
	v_mov_b32_e32 v4, v70
	v_readlane_b32 s9, v254, 12
	s_nop 0
	v_add_u32_e32 v4, 0x13f, v4
	v_mul_hi_i32 v6, v4, s8
	v_lshrrev_b32_e32 v7, 31, v6
	v_ashrrev_i32_e32 v6, 7, v6
	v_add_u32_e32 v6, v6, v7
	v_mul_lo_u32 v6, v6, s2
	v_sub_u32_e32 v6, v6, v4
	v_mov_b32_e32 v5, s9
	v_add3_u32 v3, v4, v3, v6
	ds_write_b32 v5, v3
	v_mov_b32_e32 v4, v71
	v_readlane_b32 s9, v254, 13
	s_nop 0
	v_add_u32_e32 v4, 0x13f, v4
	v_mul_hi_i32 v6, v4, s8
	v_lshrrev_b32_e32 v7, 31, v6
	v_ashrrev_i32_e32 v6, 7, v6
	v_add_u32_e32 v6, v6, v7
	v_mul_lo_u32 v6, v6, s2
	v_sub_u32_e32 v6, v6, v4
	v_mov_b32_e32 v5, s9
	v_add3_u32 v3, v4, v3, v6
	ds_write_b32 v5, v3
	v_mov_b32_e32 v4, v72
	v_readlane_b32 s9, v254, 14
	s_nop 0
	v_add_u32_e32 v4, 0x13f, v4
	v_mul_hi_i32 v6, v4, s8
	v_lshrrev_b32_e32 v7, 31, v6
	v_ashrrev_i32_e32 v6, 7, v6
	v_add_u32_e32 v6, v6, v7
	v_mul_lo_u32 v6, v6, s2
	v_sub_u32_e32 v6, v6, v4
	v_mov_b32_e32 v5, s9
	v_add3_u32 v3, v4, v3, v6
	ds_write_b32 v5, v3
	v_mov_b32_e32 v4, v73
	v_readlane_b32 s9, v254, 15
	s_nop 0
	v_add_u32_e32 v4, 0x13f, v4
	v_mul_hi_i32 v6, v4, s8
	v_lshrrev_b32_e32 v7, 31, v6
	v_ashrrev_i32_e32 v6, 7, v6
	v_add_u32_e32 v6, v6, v7
	v_mul_lo_u32 v6, v6, s2
	v_sub_u32_e32 v6, v6, v4
	v_mov_b32_e32 v5, s9
	v_add3_u32 v3, v4, v3, v6
	ds_write_b32 v5, v3
	v_mov_b32_e32 v4, v74
	v_readlane_b32 s9, v254, 16
	s_nop 0
	v_add_u32_e32 v4, 0x13f, v4
	v_mul_hi_i32 v6, v4, s8
	v_lshrrev_b32_e32 v7, 31, v6
	v_ashrrev_i32_e32 v6, 7, v6
	v_add_u32_e32 v6, v6, v7
	v_mul_lo_u32 v6, v6, s2
	v_sub_u32_e32 v6, v6, v4
	v_mov_b32_e32 v5, s9
	v_add3_u32 v3, v4, v3, v6
	ds_write_b32 v5, v3
	v_mov_b32_e32 v4, v75
	v_readlane_b32 s9, v254, 17
	s_nop 0
	v_add_u32_e32 v4, 0x13f, v4
	v_mul_hi_i32 v6, v4, s8
	v_lshrrev_b32_e32 v7, 31, v6
	v_ashrrev_i32_e32 v6, 7, v6
	v_add_u32_e32 v6, v6, v7
	v_mul_lo_u32 v6, v6, s2
	v_sub_u32_e32 v6, v6, v4
	v_mov_b32_e32 v5, s9
	v_add3_u32 v3, v4, v3, v6
	ds_write_b32 v5, v3
	v_mov_b32_e32 v4, v76
	v_readlane_b32 s9, v254, 18
	s_nop 0
	v_add_u32_e32 v4, 0x13f, v4
	v_mul_hi_i32 v6, v4, s8
	v_lshrrev_b32_e32 v7, 31, v6
	v_ashrrev_i32_e32 v6, 7, v6
	v_add_u32_e32 v6, v6, v7
	v_mul_lo_u32 v6, v6, s2
	v_sub_u32_e32 v6, v6, v4
	v_mov_b32_e32 v5, s9
	v_add3_u32 v3, v4, v3, v6
	ds_write_b32 v5, v3
	v_mov_b32_e32 v4, v77
	v_readlane_b32 s9, v254, 19
	s_nop 0
	v_add_u32_e32 v4, 0x13f, v4
	v_mul_hi_i32 v6, v4, s8
	v_lshrrev_b32_e32 v7, 31, v6
	v_ashrrev_i32_e32 v6, 7, v6
	v_add_u32_e32 v6, v6, v7
	v_mul_lo_u32 v6, v6, s2
	v_sub_u32_e32 v6, v6, v4
	v_mov_b32_e32 v5, s9
	v_add3_u32 v3, v4, v3, v6
	ds_write_b32 v5, v3
	v_mov_b32_e32 v4, v78
	v_readlane_b32 s9, v254, 20
	s_nop 0
	v_add_u32_e32 v4, 0x13f, v4
	v_mul_hi_i32 v6, v4, s8
	v_lshrrev_b32_e32 v7, 31, v6
	v_ashrrev_i32_e32 v6, 7, v6
	v_add_u32_e32 v6, v6, v7
	v_mul_lo_u32 v6, v6, s2
	v_sub_u32_e32 v6, v6, v4
	v_mov_b32_e32 v5, s9
	v_add3_u32 v3, v4, v3, v6
	ds_write_b32 v5, v3
	v_mov_b32_e32 v4, v79
	v_readlane_b32 s9, v254, 21
	s_nop 0
	v_add_u32_e32 v4, 0x13f, v4
	v_mul_hi_i32 v6, v4, s8
	v_lshrrev_b32_e32 v7, 31, v6
	v_ashrrev_i32_e32 v6, 7, v6
	v_add_u32_e32 v6, v6, v7
	v_mul_lo_u32 v6, v6, s2
	v_sub_u32_e32 v6, v6, v4
	v_mov_b32_e32 v5, s9
	v_add3_u32 v3, v4, v3, v6
	ds_write_b32 v5, v3
	v_mov_b32_e32 v4, v80
	v_readlane_b32 s9, v254, 22
	s_nop 0
	v_add_u32_e32 v4, 0x13f, v4
	v_mul_hi_i32 v6, v4, s8
	v_lshrrev_b32_e32 v7, 31, v6
	v_ashrrev_i32_e32 v6, 7, v6
	v_add_u32_e32 v6, v6, v7
	v_mul_lo_u32 v6, v6, s2
	v_sub_u32_e32 v6, v6, v4
	v_mov_b32_e32 v5, s9
	v_add3_u32 v3, v4, v3, v6
	ds_write_b32 v5, v3
	v_mov_b32_e32 v4, v81
	v_readlane_b32 s9, v254, 23
	s_nop 0
	v_add_u32_e32 v4, 0x13f, v4
	v_mul_hi_i32 v6, v4, s8
	v_lshrrev_b32_e32 v7, 31, v6
	v_ashrrev_i32_e32 v6, 7, v6
	v_add_u32_e32 v6, v6, v7
	v_mul_lo_u32 v6, v6, s2
	v_sub_u32_e32 v6, v6, v4
	v_mov_b32_e32 v5, s9
	v_add3_u32 v3, v4, v3, v6
	ds_write_b32 v5, v3
	v_mov_b32_e32 v4, v82
	v_readlane_b32 s9, v254, 24
	s_nop 0
	v_add_u32_e32 v4, 0x13f, v4
	v_mul_hi_i32 v6, v4, s8
	v_lshrrev_b32_e32 v7, 31, v6
	v_ashrrev_i32_e32 v6, 7, v6
	v_add_u32_e32 v6, v6, v7
	v_mul_lo_u32 v6, v6, s2
	v_sub_u32_e32 v6, v6, v4
	v_mov_b32_e32 v5, s9
	v_add3_u32 v3, v4, v3, v6
	ds_write_b32 v5, v3
	v_mov_b32_e32 v4, v83
	v_readlane_b32 s9, v254, 25
	s_nop 0
	v_add_u32_e32 v4, 0x13f, v4
	v_mul_hi_i32 v6, v4, s8
	v_lshrrev_b32_e32 v7, 31, v6
	v_ashrrev_i32_e32 v6, 7, v6
	v_add_u32_e32 v6, v6, v7
	v_mul_lo_u32 v6, v6, s2
	v_sub_u32_e32 v6, v6, v4
	v_mov_b32_e32 v5, s9
	v_add3_u32 v3, v4, v3, v6
	ds_write_b32 v5, v3
	v_mov_b32_e32 v4, v84
	v_readlane_b32 s9, v254, 26
	s_nop 0
	v_add_u32_e32 v4, 0x13f, v4
	v_mul_hi_i32 v6, v4, s8
	v_lshrrev_b32_e32 v7, 31, v6
	v_ashrrev_i32_e32 v6, 7, v6
	v_add_u32_e32 v6, v6, v7
	v_mul_lo_u32 v6, v6, s2
	v_sub_u32_e32 v6, v6, v4
	v_mov_b32_e32 v5, s9
	v_add3_u32 v3, v4, v3, v6
	ds_write_b32 v5, v3
	v_mov_b32_e32 v4, v85
	v_readlane_b32 s9, v254, 27
	s_nop 0
	v_add_u32_e32 v4, 0x13f, v4
	v_mul_hi_i32 v6, v4, s8
	v_lshrrev_b32_e32 v7, 31, v6
	v_ashrrev_i32_e32 v6, 7, v6
	v_add_u32_e32 v6, v6, v7
	v_mul_lo_u32 v6, v6, s2
	v_sub_u32_e32 v6, v6, v4
	v_mov_b32_e32 v5, s9
	v_add3_u32 v3, v4, v3, v6
	ds_write_b32 v5, v3
	v_mov_b32_e32 v4, v86
	v_readlane_b32 s9, v254, 28
	s_nop 0
	v_add_u32_e32 v4, 0x13f, v4
	v_mul_hi_i32 v6, v4, s8
	v_lshrrev_b32_e32 v7, 31, v6
	v_ashrrev_i32_e32 v6, 7, v6
	v_add_u32_e32 v6, v6, v7
	v_mul_lo_u32 v6, v6, s2
	v_sub_u32_e32 v6, v6, v4
	v_mov_b32_e32 v5, s9
	v_add3_u32 v3, v4, v3, v6
	ds_write_b32 v5, v3
	v_mov_b32_e32 v4, v87
	v_readlane_b32 s9, v254, 29
	s_nop 0
	v_add_u32_e32 v4, 0x13f, v4
	v_mul_hi_i32 v6, v4, s8
	v_lshrrev_b32_e32 v7, 31, v6
	v_ashrrev_i32_e32 v6, 7, v6
	v_add_u32_e32 v6, v6, v7
	v_mul_lo_u32 v6, v6, s2
	v_sub_u32_e32 v6, v6, v4
	v_mov_b32_e32 v5, s9
	v_add3_u32 v3, v4, v3, v6
	ds_write_b32 v5, v3
	v_mov_b32_e32 v4, v88
	v_readlane_b32 s9, v254, 30
	s_nop 0
	v_add_u32_e32 v4, 0x13f, v4
	v_mul_hi_i32 v6, v4, s8
	v_lshrrev_b32_e32 v7, 31, v6
	v_ashrrev_i32_e32 v6, 7, v6
	v_add_u32_e32 v6, v6, v7
	v_mul_lo_u32 v6, v6, s2
	v_sub_u32_e32 v6, v6, v4
	v_mov_b32_e32 v5, s9
	v_add3_u32 v3, v4, v3, v6
	ds_write_b32 v5, v3
	v_mov_b32_e32 v4, v89
	v_readlane_b32 s9, v254, 31
	s_nop 0
	v_add_u32_e32 v4, 0x13f, v4
	v_mul_hi_i32 v6, v4, s8
	v_lshrrev_b32_e32 v7, 31, v6
	v_ashrrev_i32_e32 v6, 7, v6
	v_add_u32_e32 v6, v6, v7
	v_mul_lo_u32 v6, v6, s2
	v_sub_u32_e32 v6, v6, v4
	v_mov_b32_e32 v5, s9
	v_add3_u32 v3, v4, v3, v6
	ds_write_b32 v5, v3
	v_mov_b32_e32 v4, v90
	v_readlane_b32 s9, v254, 32
	s_nop 0
	v_add_u32_e32 v4, 0x13f, v4
	v_mul_hi_i32 v6, v4, s8
	v_lshrrev_b32_e32 v7, 31, v6
	v_ashrrev_i32_e32 v6, 7, v6
	v_add_u32_e32 v6, v6, v7
	v_mul_lo_u32 v6, v6, s2
	v_sub_u32_e32 v6, v6, v4
	v_mov_b32_e32 v5, s9
	v_add3_u32 v3, v4, v3, v6
	ds_write_b32 v5, v3
	v_mov_b32_e32 v4, v91
	v_readlane_b32 s9, v254, 33
	s_nop 0
	v_add_u32_e32 v4, 0x13f, v4
	v_mul_hi_i32 v6, v4, s8
	v_lshrrev_b32_e32 v7, 31, v6
	v_ashrrev_i32_e32 v6, 7, v6
	v_add_u32_e32 v6, v6, v7
	v_mul_lo_u32 v6, v6, s2
	v_sub_u32_e32 v6, v6, v4
	v_mov_b32_e32 v5, s9
	v_add3_u32 v3, v4, v3, v6
	ds_write_b32 v5, v3
	v_mov_b32_e32 v4, v92
	v_readlane_b32 s9, v254, 34
	s_nop 0
	v_add_u32_e32 v4, 0x13f, v4
	v_mul_hi_i32 v6, v4, s8
	v_lshrrev_b32_e32 v7, 31, v6
	v_ashrrev_i32_e32 v6, 7, v6
	v_add_u32_e32 v6, v6, v7
	v_mul_lo_u32 v6, v6, s2
	v_sub_u32_e32 v6, v6, v4
	v_mov_b32_e32 v5, s9
	v_add3_u32 v3, v4, v3, v6
	ds_write_b32 v5, v3
	v_mov_b32_e32 v4, v93
	v_readlane_b32 s9, v254, 35
	s_nop 0
	v_add_u32_e32 v4, 0x13f, v4
	v_mul_hi_i32 v6, v4, s8
	v_lshrrev_b32_e32 v7, 31, v6
	v_ashrrev_i32_e32 v6, 7, v6
	v_add_u32_e32 v6, v6, v7
	v_mul_lo_u32 v6, v6, s2
	v_sub_u32_e32 v6, v6, v4
	v_mov_b32_e32 v5, s9
	v_add3_u32 v3, v4, v3, v6
	ds_write_b32 v5, v3
	v_mov_b32_e32 v4, v94
	v_readlane_b32 s9, v254, 36
	s_nop 0
	v_add_u32_e32 v4, 0x13f, v4
	v_mul_hi_i32 v6, v4, s8
	v_lshrrev_b32_e32 v7, 31, v6
	v_ashrrev_i32_e32 v6, 7, v6
	v_add_u32_e32 v6, v6, v7
	v_mul_lo_u32 v6, v6, s2
	v_sub_u32_e32 v6, v6, v4
	v_mov_b32_e32 v5, s9
	v_add3_u32 v3, v4, v3, v6
	ds_write_b32 v5, v3
	v_mov_b32_e32 v4, v95
	v_readlane_b32 s9, v254, 37
	s_nop 0
	v_add_u32_e32 v4, 0x13f, v4
	v_mul_hi_i32 v6, v4, s8
	v_lshrrev_b32_e32 v7, 31, v6
	v_ashrrev_i32_e32 v6, 7, v6
	v_add_u32_e32 v6, v6, v7
	v_mul_lo_u32 v6, v6, s2
	v_sub_u32_e32 v6, v6, v4
	v_mov_b32_e32 v5, s9
	v_add3_u32 v3, v4, v3, v6
	ds_write_b32 v5, v3
	v_mov_b32_e32 v4, v96
	v_readlane_b32 s9, v254, 38
	s_nop 0
	v_add_u32_e32 v4, 0x13f, v4
	v_mul_hi_i32 v6, v4, s8
	v_lshrrev_b32_e32 v7, 31, v6
	v_ashrrev_i32_e32 v6, 7, v6
	v_add_u32_e32 v6, v6, v7
	v_mul_lo_u32 v6, v6, s2
	v_sub_u32_e32 v6, v6, v4
	v_mov_b32_e32 v5, s9
	v_add3_u32 v3, v4, v3, v6
	ds_write_b32 v5, v3
	v_mov_b32_e32 v4, v97
	v_readlane_b32 s9, v254, 39
	s_nop 0
	v_add_u32_e32 v4, 0x13f, v4
	v_mul_hi_i32 v6, v4, s8
	v_lshrrev_b32_e32 v7, 31, v6
	v_ashrrev_i32_e32 v6, 7, v6
	v_add_u32_e32 v6, v6, v7
	v_mul_lo_u32 v6, v6, s2
	v_sub_u32_e32 v6, v6, v4
	v_mov_b32_e32 v5, s9
	v_add3_u32 v3, v4, v3, v6
	ds_write_b32 v5, v3
	v_mov_b32_e32 v4, v98
	v_readlane_b32 s9, v254, 40
	s_nop 0
	v_add_u32_e32 v4, 0x13f, v4
	v_mul_hi_i32 v6, v4, s8
	v_lshrrev_b32_e32 v7, 31, v6
	v_ashrrev_i32_e32 v6, 7, v6
	v_add_u32_e32 v6, v6, v7
	v_mul_lo_u32 v6, v6, s2
	v_sub_u32_e32 v6, v6, v4
	v_mov_b32_e32 v5, s9
	v_add3_u32 v3, v4, v3, v6
	ds_write_b32 v5, v3
	v_mov_b32_e32 v4, v99
	v_readlane_b32 s9, v254, 41
	s_nop 0
	v_add_u32_e32 v4, 0x13f, v4
	v_mul_hi_i32 v6, v4, s8
	v_lshrrev_b32_e32 v7, 31, v6
	v_ashrrev_i32_e32 v6, 7, v6
	v_add_u32_e32 v6, v6, v7
	v_mul_lo_u32 v6, v6, s2
	v_sub_u32_e32 v6, v6, v4
	v_mov_b32_e32 v5, s9
	v_add3_u32 v3, v4, v3, v6
	ds_write_b32 v5, v3
	v_mov_b32_e32 v4, v100
	v_readlane_b32 s9, v254, 42
	s_nop 0
	v_add_u32_e32 v4, 0x13f, v4
	v_mul_hi_i32 v6, v4, s8
	v_lshrrev_b32_e32 v7, 31, v6
	v_ashrrev_i32_e32 v6, 7, v6
	v_add_u32_e32 v6, v6, v7
	v_mul_lo_u32 v6, v6, s2
	v_sub_u32_e32 v6, v6, v4
	v_mov_b32_e32 v5, s9
	v_add3_u32 v3, v4, v3, v6
	ds_write_b32 v5, v3
	v_mov_b32_e32 v4, v101
	v_readlane_b32 s9, v254, 43
	s_nop 0
	v_add_u32_e32 v4, 0x13f, v4
	v_mul_hi_i32 v6, v4, s8
	v_lshrrev_b32_e32 v7, 31, v6
	v_ashrrev_i32_e32 v6, 7, v6
	v_add_u32_e32 v6, v6, v7
	v_mul_lo_u32 v6, v6, s2
	v_sub_u32_e32 v6, v6, v4
	v_mov_b32_e32 v5, s9
	v_add3_u32 v3, v4, v3, v6
	ds_write_b32 v5, v3
	v_mov_b32_e32 v4, v102
	v_readlane_b32 s9, v254, 44
	s_nop 0
	v_add_u32_e32 v4, 0x13f, v4
	v_mul_hi_i32 v6, v4, s8
	v_lshrrev_b32_e32 v7, 31, v6
	v_ashrrev_i32_e32 v6, 7, v6
	v_add_u32_e32 v6, v6, v7
	v_mul_lo_u32 v6, v6, s2
	v_sub_u32_e32 v6, v6, v4
	v_mov_b32_e32 v5, s9
	v_add3_u32 v3, v4, v3, v6
	ds_write_b32 v5, v3
	v_mov_b32_e32 v4, v103
	v_readlane_b32 s9, v254, 45
	s_nop 0
	v_add_u32_e32 v4, 0x13f, v4
	v_mul_hi_i32 v6, v4, s8
	v_lshrrev_b32_e32 v7, 31, v6
	v_ashrrev_i32_e32 v6, 7, v6
	v_add_u32_e32 v6, v6, v7
	v_mul_lo_u32 v6, v6, s2
	v_sub_u32_e32 v6, v6, v4
	v_mov_b32_e32 v5, s9
	v_add3_u32 v3, v4, v3, v6
	ds_write_b32 v5, v3
	v_mov_b32_e32 v4, v104
	v_readlane_b32 s9, v254, 46
	s_nop 0
	v_add_u32_e32 v4, 0x13f, v4
	v_mul_hi_i32 v6, v4, s8
	v_lshrrev_b32_e32 v7, 31, v6
	v_ashrrev_i32_e32 v6, 7, v6
	v_add_u32_e32 v6, v6, v7
	v_mul_lo_u32 v6, v6, s2
	v_sub_u32_e32 v6, v6, v4
	v_mov_b32_e32 v5, s9
	v_add3_u32 v3, v4, v3, v6
	ds_write_b32 v5, v3
	v_mov_b32_e32 v4, v105
	v_readlane_b32 s9, v254, 47
	s_nop 0
	v_add_u32_e32 v4, 0x13f, v4
	v_mul_hi_i32 v6, v4, s8
	v_lshrrev_b32_e32 v7, 31, v6
	v_ashrrev_i32_e32 v6, 7, v6
	v_add_u32_e32 v6, v6, v7
	v_mul_lo_u32 v6, v6, s2
	v_sub_u32_e32 v6, v6, v4
	v_mov_b32_e32 v5, s9
	v_add3_u32 v3, v4, v3, v6
	ds_write_b32 v5, v3
	v_mov_b32_e32 v4, v106
	v_readlane_b32 s9, v254, 48
	s_nop 0
	v_add_u32_e32 v4, 0x13f, v4
	v_mul_hi_i32 v6, v4, s8
	v_lshrrev_b32_e32 v7, 31, v6
	v_ashrrev_i32_e32 v6, 7, v6
	v_add_u32_e32 v6, v6, v7
	v_mul_lo_u32 v6, v6, s2
	v_sub_u32_e32 v6, v6, v4
	v_mov_b32_e32 v5, s9
	v_add3_u32 v3, v4, v3, v6
	ds_write_b32 v5, v3
	v_mov_b32_e32 v4, v107
	v_readlane_b32 s9, v254, 49
	s_nop 0
	v_add_u32_e32 v4, 0x13f, v4
	v_mul_hi_i32 v6, v4, s8
	v_lshrrev_b32_e32 v7, 31, v6
	v_ashrrev_i32_e32 v6, 7, v6
	v_add_u32_e32 v6, v6, v7
	v_mul_lo_u32 v6, v6, s2
	v_sub_u32_e32 v6, v6, v4
	v_mov_b32_e32 v5, s9
	v_add3_u32 v3, v4, v3, v6
	ds_write_b32 v5, v3
	v_mov_b32_e32 v4, v108
	v_readlane_b32 s9, v254, 50
	s_nop 0
	v_add_u32_e32 v4, 0x13f, v4
	v_mul_hi_i32 v6, v4, s8
	v_lshrrev_b32_e32 v7, 31, v6
	v_ashrrev_i32_e32 v6, 7, v6
	v_add_u32_e32 v6, v6, v7
	v_mul_lo_u32 v6, v6, s2
	v_sub_u32_e32 v6, v6, v4
	v_mov_b32_e32 v5, s9
	v_add3_u32 v3, v4, v3, v6
	ds_write_b32 v5, v3
	v_mov_b32_e32 v4, v109
	v_readlane_b32 s9, v254, 51
	s_nop 0
	v_add_u32_e32 v4, 0x13f, v4
	v_mul_hi_i32 v6, v4, s8
	v_lshrrev_b32_e32 v7, 31, v6
	v_ashrrev_i32_e32 v6, 7, v6
	v_add_u32_e32 v6, v6, v7
	v_mul_lo_u32 v6, v6, s2
	v_sub_u32_e32 v6, v6, v4
	v_mov_b32_e32 v5, s9
	v_add3_u32 v3, v4, v3, v6
	ds_write_b32 v5, v3
	v_mov_b32_e32 v4, v110
	v_readlane_b32 s9, v254, 52
	s_nop 0
	v_add_u32_e32 v4, 0x13f, v4
	v_mul_hi_i32 v6, v4, s8
	v_lshrrev_b32_e32 v7, 31, v6
	v_ashrrev_i32_e32 v6, 7, v6
	v_add_u32_e32 v6, v6, v7
	v_mul_lo_u32 v6, v6, s2
	v_sub_u32_e32 v6, v6, v4
	v_mov_b32_e32 v5, s9
	v_add3_u32 v3, v4, v3, v6
	ds_write_b32 v5, v3
	v_mov_b32_e32 v4, v111
	v_readlane_b32 s9, v254, 53
	s_nop 0
	v_add_u32_e32 v4, 0x13f, v4
	v_mul_hi_i32 v6, v4, s8
	v_lshrrev_b32_e32 v7, 31, v6
	v_ashrrev_i32_e32 v6, 7, v6
	v_add_u32_e32 v6, v6, v7
	v_mul_lo_u32 v6, v6, s2
	v_sub_u32_e32 v6, v6, v4
	v_mov_b32_e32 v5, s9
	v_add3_u32 v3, v4, v3, v6
	ds_write_b32 v5, v3
	v_mov_b32_e32 v4, v112
	v_readlane_b32 s9, v254, 54
	s_nop 0
	v_add_u32_e32 v4, 0x13f, v4
	v_mul_hi_i32 v6, v4, s8
	v_lshrrev_b32_e32 v7, 31, v6
	v_ashrrev_i32_e32 v6, 7, v6
	v_add_u32_e32 v6, v6, v7
	v_mul_lo_u32 v6, v6, s2
	v_sub_u32_e32 v6, v6, v4
	v_mov_b32_e32 v5, s9
	v_add3_u32 v3, v4, v3, v6
	ds_write_b32 v5, v3
	v_mov_b32_e32 v4, v113
	v_readlane_b32 s9, v254, 55
	s_nop 0
	v_add_u32_e32 v4, 0x13f, v4
	v_mul_hi_i32 v6, v4, s8
	v_lshrrev_b32_e32 v7, 31, v6
	v_ashrrev_i32_e32 v6, 7, v6
	v_add_u32_e32 v6, v6, v7
	v_mul_lo_u32 v6, v6, s2
	v_sub_u32_e32 v6, v6, v4
	v_mov_b32_e32 v5, s9
	v_add3_u32 v3, v4, v3, v6
	ds_write_b32 v5, v3
	v_mov_b32_e32 v4, v114
	v_readlane_b32 s9, v254, 56
	s_nop 0
	v_add_u32_e32 v4, 0x13f, v4
	v_mul_hi_i32 v6, v4, s8
	v_lshrrev_b32_e32 v7, 31, v6
	v_ashrrev_i32_e32 v6, 7, v6
	v_add_u32_e32 v6, v6, v7
	v_mul_lo_u32 v6, v6, s2
	v_sub_u32_e32 v6, v6, v4
	v_mov_b32_e32 v5, s9
	v_add3_u32 v3, v4, v3, v6
	ds_write_b32 v5, v3
	v_mov_b32_e32 v4, v115
	v_readlane_b32 s9, v254, 57
	s_nop 0
	v_add_u32_e32 v4, 0x13f, v4
	v_mul_hi_i32 v6, v4, s8
	v_lshrrev_b32_e32 v7, 31, v6
	v_ashrrev_i32_e32 v6, 7, v6
	v_add_u32_e32 v6, v6, v7
	v_mul_lo_u32 v6, v6, s2
	v_sub_u32_e32 v6, v6, v4
	v_mov_b32_e32 v5, s9
	v_add3_u32 v3, v4, v3, v6
	ds_write_b32 v5, v3
	v_mov_b32_e32 v4, v116
	v_readlane_b32 s9, v254, 58
	s_nop 0
	v_add_u32_e32 v4, 0x13f, v4
	v_mul_hi_i32 v6, v4, s8
	v_lshrrev_b32_e32 v7, 31, v6
	v_ashrrev_i32_e32 v6, 7, v6
	v_add_u32_e32 v6, v6, v7
	v_mul_lo_u32 v6, v6, s2
	v_sub_u32_e32 v6, v6, v4
	v_mov_b32_e32 v5, s9
	v_add3_u32 v3, v4, v3, v6
	ds_write_b32 v5, v3
	v_mov_b32_e32 v4, v117
	v_readlane_b32 s9, v254, 59
	s_nop 0
	v_add_u32_e32 v4, 0x13f, v4
	v_mul_hi_i32 v6, v4, s8
	v_lshrrev_b32_e32 v7, 31, v6
	v_ashrrev_i32_e32 v6, 7, v6
	v_add_u32_e32 v6, v6, v7
	v_mul_lo_u32 v6, v6, s2
	v_sub_u32_e32 v6, v6, v4
	v_mov_b32_e32 v5, s9
	v_add3_u32 v3, v4, v3, v6
	ds_write_b32 v5, v3
	v_mov_b32_e32 v4, v118
	v_readlane_b32 s9, v254, 60
	s_nop 0
	v_add_u32_e32 v4, 0x13f, v4
	v_mul_hi_i32 v6, v4, s8
	v_lshrrev_b32_e32 v7, 31, v6
	v_ashrrev_i32_e32 v6, 7, v6
	v_add_u32_e32 v6, v6, v7
	v_mul_lo_u32 v6, v6, s2
	v_sub_u32_e32 v6, v6, v4
	v_mov_b32_e32 v5, s9
	v_add3_u32 v3, v4, v3, v6
	ds_write_b32 v5, v3
	v_mov_b32_e32 v4, v119
	v_readlane_b32 s9, v254, 61
	s_nop 0
	v_add_u32_e32 v4, 0x13f, v4
	v_mul_hi_i32 v6, v4, s8
	v_lshrrev_b32_e32 v7, 31, v6
	v_ashrrev_i32_e32 v6, 7, v6
	v_add_u32_e32 v6, v6, v7
	v_mul_lo_u32 v6, v6, s2
	v_sub_u32_e32 v6, v6, v4
	v_mov_b32_e32 v5, s9
	v_add3_u32 v3, v4, v3, v6
	ds_write_b32 v5, v3
	v_mov_b32_e32 v4, v120
	v_readlane_b32 s9, v254, 62
	s_nop 0
	v_add_u32_e32 v4, 0x13f, v4
	v_mul_hi_i32 v6, v4, s8
	v_lshrrev_b32_e32 v7, 31, v6
	v_ashrrev_i32_e32 v6, 7, v6
	v_add_u32_e32 v6, v6, v7
	v_mul_lo_u32 v6, v6, s2
	v_sub_u32_e32 v6, v6, v4
	v_mov_b32_e32 v5, s9
	v_add3_u32 v3, v4, v3, v6
	ds_write_b32 v5, v3
	v_mov_b32_e32 v4, v121
	v_readlane_b32 s9, v254, 63
	s_nop 0
	v_add_u32_e32 v4, 0x13f, v4
	v_mul_hi_i32 v6, v4, s8
	v_lshrrev_b32_e32 v7, 31, v6
	v_ashrrev_i32_e32 v6, 7, v6
	v_add_u32_e32 v6, v6, v7
	v_mul_lo_u32 v6, v6, s2
	v_sub_u32_e32 v6, v6, v4
	v_mov_b32_e32 v5, s9
	v_add3_u32 v3, v4, v3, v6
	ds_write_b32 v5, v3
	v_mov_b32_e32 v4, v122
	v_readlane_b32 s9, v255, 0
	s_nop 0
	v_add_u32_e32 v4, 0x13f, v4
	v_mul_hi_i32 v6, v4, s8
	v_lshrrev_b32_e32 v7, 31, v6
	v_ashrrev_i32_e32 v6, 7, v6
	v_add_u32_e32 v6, v6, v7
	v_mul_lo_u32 v6, v6, s2
	v_sub_u32_e32 v6, v6, v4
	v_mov_b32_e32 v5, s9
	v_add3_u32 v3, v4, v3, v6
	ds_write_b32 v5, v3
	v_mov_b32_e32 v4, v123
	v_readlane_b32 s9, v255, 1
	s_nop 0
	v_add_u32_e32 v4, 0x13f, v4
	v_mul_hi_i32 v6, v4, s8
	v_lshrrev_b32_e32 v7, 31, v6
	v_ashrrev_i32_e32 v6, 7, v6
	v_add_u32_e32 v6, v6, v7
	v_mul_lo_u32 v6, v6, s2
	v_sub_u32_e32 v6, v6, v4
	v_mov_b32_e32 v5, s9
	v_add3_u32 v3, v4, v3, v6
	ds_write_b32 v5, v3
	v_mov_b32_e32 v4, v124
	v_readlane_b32 s9, v255, 2
	s_nop 0
	v_add_u32_e32 v4, 0x13f, v4
	v_mul_hi_i32 v6, v4, s8
	v_lshrrev_b32_e32 v7, 31, v6
	v_ashrrev_i32_e32 v6, 7, v6
	v_add_u32_e32 v6, v6, v7
	v_mul_lo_u32 v6, v6, s2
	v_sub_u32_e32 v6, v6, v4
	v_mov_b32_e32 v5, s9
	v_add3_u32 v3, v4, v3, v6
	ds_write_b32 v5, v3
	v_mov_b32_e32 v4, v125
	v_readlane_b32 s9, v255, 3
	s_nop 0
	v_add_u32_e32 v4, 0x13f, v4
	v_mul_hi_i32 v6, v4, s8
	v_lshrrev_b32_e32 v7, 31, v6
	v_ashrrev_i32_e32 v6, 7, v6
	v_add_u32_e32 v6, v6, v7
	v_mul_lo_u32 v6, v6, s2
	v_sub_u32_e32 v6, v6, v4
	v_mov_b32_e32 v5, s9
	v_add3_u32 v3, v4, v3, v6
	ds_write_b32 v5, v3
	v_mov_b32_e32 v4, v126
	v_readlane_b32 s9, v255, 4
	s_nop 0
	v_add_u32_e32 v4, 0x13f, v4
	v_mul_hi_i32 v6, v4, s8
	v_lshrrev_b32_e32 v7, 31, v6
	v_ashrrev_i32_e32 v6, 7, v6
	v_add_u32_e32 v6, v6, v7
	v_mul_lo_u32 v6, v6, s2
	v_sub_u32_e32 v6, v6, v4
	v_mov_b32_e32 v5, s9
	v_add3_u32 v3, v4, v3, v6
	ds_write_b32 v5, v3
	v_mov_b32_e32 v4, v127
	v_readlane_b32 s9, v255, 5
	s_nop 0
	v_add_u32_e32 v4, 0x13f, v4
	v_mul_hi_i32 v6, v4, s8
	v_lshrrev_b32_e32 v7, 31, v6
	v_ashrrev_i32_e32 v6, 7, v6
	v_add_u32_e32 v6, v6, v7
	v_mul_lo_u32 v6, v6, s2
	v_sub_u32_e32 v6, v6, v4
	v_mov_b32_e32 v5, s9
	v_add3_u32 v3, v4, v3, v6
	ds_write_b32 v5, v3
	v_mov_b32_e32 v4, v128
	v_readlane_b32 s9, v255, 6
	s_nop 0
	v_add_u32_e32 v4, 0x13f, v4
	v_mul_hi_i32 v6, v4, s8
	v_lshrrev_b32_e32 v7, 31, v6
	v_ashrrev_i32_e32 v6, 7, v6
	v_add_u32_e32 v6, v6, v7
	v_mul_lo_u32 v6, v6, s2
	v_sub_u32_e32 v6, v6, v4
	v_mov_b32_e32 v5, s9
	v_add3_u32 v3, v4, v3, v6
	ds_write_b32 v5, v3
	v_mov_b32_e32 v4, v129
	v_readlane_b32 s9, v255, 7
	s_nop 0
	v_add_u32_e32 v4, 0x13f, v4
	v_mul_hi_i32 v6, v4, s8
	v_lshrrev_b32_e32 v7, 31, v6
	v_ashrrev_i32_e32 v6, 7, v6
	v_add_u32_e32 v6, v6, v7
	v_mul_lo_u32 v6, v6, s2
	v_sub_u32_e32 v6, v6, v4
	v_mov_b32_e32 v5, s9
	v_add3_u32 v3, v4, v3, v6
	ds_write_b32 v5, v3
	v_mov_b32_e32 v4, v130
	v_readlane_b32 s9, v255, 8
	s_nop 0
	v_add_u32_e32 v4, 0x13f, v4
	v_mul_hi_i32 v6, v4, s8
	v_lshrrev_b32_e32 v7, 31, v6
	v_ashrrev_i32_e32 v6, 7, v6
	v_add_u32_e32 v6, v6, v7
	v_mul_lo_u32 v6, v6, s2
	v_sub_u32_e32 v6, v6, v4
	v_mov_b32_e32 v5, s9
	v_add3_u32 v3, v4, v3, v6
	ds_write_b32 v5, v3
	v_mov_b32_e32 v0, v131
	s_nop 0
	v_add_u32_e32 v0, 0x13f, v0
	v_mul_hi_i32 v1, v0, s8
	v_lshrrev_b32_e32 v4, 31, v1
	v_ashrrev_i32_e32 v1, 7, v1
	v_add_u32_e32 v1, v1, v4
	v_mul_lo_u32 v1, v1, s2
	v_sub_u32_e32 v1, v1, v0
	v_readlane_b32 s2, v254, 2
	v_add3_u32 v0, v0, v3, v1
	s_nop 0
	v_mov_b32_e32 v1, s2
	ds_write_b32 v1, v0

.LBB0_997:
	s_or_b64 exec, exec, s[64:65]
	s_mov_b32 s0, s37
	s_waitcnt lgkmcnt(0)
	s_barrier
	s_mov_b32 s1, s33
	v_mbcnt_lo_u32_b32 v0, -1, s0
	v_mbcnt_hi_u32_b32 v0, -1, v0
	v_lshl_or_b32 v0, s1, 6, v0
	v_readlane_b32 s0, v254, 0
	s_mov_b32 s16, s0
	s_mov_b32 s0, s37
	s_add_i32 s0, s0, 0x20120
	v_mov_b32_e32 v1, s0
	s_mov_b32 s0, 0
	v_mov_b32_e32 v251, 0x20000
	ds_read_b64 v[206:207], v251 offset:288
	ds_read_b64 v[208:209], v251 offset:224
	ds_read_b64 v[210:211], v251 offset:232
	ds_read_b64 v[212:213], v251 offset:288
	s_add_i32 s0, s0, 0x200e0
	v_mov_b32_e32 v1, s0
	s_mov_b32 s0, s60
	s_mov_b32 s5, 0
	s_add_i32 s5, s5, 0x200e8
	v_readlane_b32 s1, v254, 1
	v_mov_b32_e32 v1, s5
	s_mov_b32 s8, s60
	s_mov_b32 s5, 0
	s_waitcnt lgkmcnt(0)
	v_readfirstlane_b32 s1, v207
	v_readfirstlane_b32 s4, v206
	s_add_i32 s5, s5, 0x20120
	v_mov_b32_e32 v1, s5
	v_readlane_b32 s5, v255, 10
	v_readfirstlane_b32 s2, v209
	v_readfirstlane_b32 s6, v208
	v_mov_b32_e32 v1, s5
	ds_read_b32 v158, v1
	s_waitcnt lgkmcnt(0)
	v_readfirstlane_b32 s10, v211
	v_readfirstlane_b32 s14, v210
	v_readfirstlane_b32 s11, v213
	v_readfirstlane_b32 s13, v212
	v_readfirstlane_b32 s5, v158
	s_lshl_b32 s5, s5, 3
	s_add_i32 s17, s5, 56
	s_andn2_b32 s17, s17, 63
	s_cmp_ge_i32 s16, s17
	v_readfirstlane_b32 s12, v0
	s_cbranch_scc1 .LBB0_1004
	s_add_u32 s4, s4, 0x1e79fd00
	s_addc_u32 s5, s1, 0
	s_ashr_i32 s1, s0, 31
	s_lshl_b64 s[0:1], s[0:1], 28
	s_add_u32 s6, s6, s0
	s_addc_u32 s7, s2, s1
	s_ashr_i32 s9, s8, 31
	s_lshl_b64 s[0:1], s[8:9], 28
	s_add_u32 s8, s14, s0
	s_addc_u32 s9, s10, s1
	s_add_u32 s10, s13, 0x2779fd00
	s_addc_u32 s11, s11, 0
	s_ashr_i32 s2, s12, 6
	v_bfe_u32 v2, v0, 4, 2
	v_and_b32_e32 v3, 7, v0
	s_lshl_b32 s0, s2, 5
	v_bitop3_b32 v3, v2, v3, 4 bitop3:0x36
	v_bitop3_b32 v2, v2, v0, 7 bitop3:0x78
	s_and_b32 s14, s0, 32
	s_ashr_i32 s0, s12, 7
	v_and_b32_e32 v1, 63, v0
	v_lshlrev_b32_e32 v161, 4, v2
	v_and_b32_e32 v2, 15, v0
	s_mulk_i32 s0, 0x50
	v_lshlrev_b32_e32 v160, 4, v3
	v_or_b32_e32 v3, s14, v2
	v_or_b32_e32 v162, s0, v2
	v_lshlrev_b32_e32 v2, 1, v1
	v_or_b32_e32 v4, 1, v2
	v_bitop3_b32 v5, s2, v4, 7 bitop3:0x78
	v_lshlrev_b32_e32 v4, 7, v4
	v_ashrrev_i32_e32 v159, 3, v0
	v_lshl_add_u32 v163, v5, 4, v4
	v_bitop3_b32 v2, s2, v2, 6 bitop3:0x78
	v_lshlrev_b32_e32 v4, 8, v1
	v_lshl_add_u32 v164, v2, 4, v4
	v_xor_b32_e32 v2, v159, v0
	v_lshlrev_b32_e32 v2, 4, v2
	v_lshlrev_b32_e32 v4, 7, v159
	s_movk_i32 s0, 0x70
	v_and_or_b32 v5, v2, s0, v4
	v_lshlrev_b32_e32 v2, 3, v0
	v_cmp_lt_u32_e64 s[0:1], 31, v1
	v_lshlrev_b32_e32 v1, 1, v0
	s_lshl_b32 s12, s2, 3
	v_and_b32_e32 v6, 16, v0
	v_lshrrev_b32_e32 v0, 2, v0
	v_lshlrev_b32_e32 v3, 7, v3
	v_and_b32_e32 v2, 56, v2
	v_and_b32_e32 v4, 62, v1
	s_ashr_i32 s13, s12, 31
	v_add_u32_e32 v165, 0, v5
	s_add_i32 s18, 0, 0x18000
	v_and_b32_e32 v0, 8, v0
	s_lshl_b64 s[12:13], s[12:13], 11
	v_add_u32_e32 v166, s66, v3
	v_lshl_add_u32 v167, v162, 7, 0
	v_add_u32_e32 v168, 0xa000, v165
	v_add_u32_e32 v169, s18, v3
	v_lshlrev_b32_e32 v100, 1, v2
	v_lshlrev_b32_e32 v102, 2, v4
	s_lshl_b32 s19, s14, 1
	v_lshlrev_b32_e32 v104, 1, v6
	v_lshlrev_b32_e32 v106, 1, v0
	v_mbcnt_lo_u32_b32 v184, -1, 0
	v_mbcnt_hi_u32_b32 v184, -1, v184
	v_and_b32_e32 v185, 31, v184
	v_lshrrev_b32_e32 v186, 5, v184
	v_cmp_lt_u32_e64 s[0:1], 15, v185
	v_and_b32_e32 v187, 15, v185
	v_lshlrev_b32_e32 v187, 4, v187
	v_lshl_add_u32 v102, v186, 13, v187
	v_lshlrev_b32_e32 v188, 2, v185
	v_lshl_add_u32 v188, v186, 1, v188
	v_and_b32_e32 v189, 7, v188
	v_xor_b32_e32 v189, s33, v189
	v_lshlrev_b32_e32 v189, 4, v189
	v_lshl_add_u32 v164, v188, 7, v189
	v_add_u32_e32 v188, 1, v188
	v_and_b32_e32 v189, 7, v188
	v_xor_b32_e32 v189, s33, v189
	v_lshlrev_b32_e32 v189, 4, v189
	v_lshl_add_u32 v163, v188, 7, v189
	s_branch .LBB0_1000

.LBB0_1048:
	s_or_b64 exec, exec, s[64:65]
	s_mov_b32 s0, s37
	s_waitcnt lgkmcnt(0)
	s_barrier
	s_mov_b32 s1, s33
	v_mbcnt_lo_u32_b32 v0, -1, s0
	v_mbcnt_hi_u32_b32 v0, -1, v0
	v_lshl_or_b32 v0, s1, 6, v0
	v_readlane_b32 s0, v254, 0
	s_mov_b32 s16, s0
	s_mov_b32 s0, s37
	s_add_i32 s0, s0, 0x20120
	v_mov_b32_e32 v1, s0
	s_mov_b32 s0, 0
	v_mov_b32_e32 v251, 0x20000
	ds_read_b64 v[206:207], v251 offset:288
	ds_read_b64 v[208:209], v251 offset:240
	ds_read_b64 v[210:211], v251 offset:288
	ds_read_b64 v[212:213], v251 offset:288
	s_add_i32 s0, s0, 0x200f0
	v_mov_b32_e32 v1, s0
	s_mov_b32 s4, s60
	s_mov_b32 s5, 0
	s_add_i32 s5, s5, 0x20120
	v_readlane_b32 s1, v254, 1
	v_mov_b32_e32 v1, s5
	s_mov_b32 s5, 0
	s_waitcnt lgkmcnt(0)
	v_readfirstlane_b32 s1, v207
	v_readfirstlane_b32 s0, v206
	s_add_i32 s5, s5, 0x20120
	v_mov_b32_e32 v1, s5
	v_readlane_b32 s5, v255, 10
	v_readfirstlane_b32 s2, v209
	v_readfirstlane_b32 s6, v208
	v_mov_b32_e32 v1, s5
	ds_read_b32 v158, v1
	s_waitcnt lgkmcnt(0)
	v_readfirstlane_b32 s7, v211
	v_readfirstlane_b32 s11, v210
	v_readfirstlane_b32 s9, v213
	v_readfirstlane_b32 s8, v212
	v_readfirstlane_b32 s5, v158
	s_lshl_b32 s5, s5, 4
	s_addk_i32 s5, 0x70
	s_and_b32 s17, s5, 0xffffff80
	s_cmp_ge_i32 s16, s17
	v_readfirstlane_b32 s10, v0
	s_cbranch_scc1 .LBB0_1055
	v_readfirstlane_b32 s30, v158
	s_mov_b32 s26, 0
	s_mov_b32 s27, 0
	s_mov_b32 s28, 0
	s_mov_b32 s29, 0
	s_lshr_b32 s31, s16, 6
	s_bfe_u32 s38, s16, 0x30003
	s_and_b32 s39, s16, 7
	s_sub_i32 s32, s30, 64
	s_max_i32 s32, s32, 0
	s_min_i32 s32, s32, 8
	s_lshl_b32 s35, s32, 3
	s_add_u32 s29, s29, s35
	s_cmp_lt_u32 s31, 1
	s_cbranch_scc1 .Lremap_g0_notbelow
	s_add_u32 s28, s28, s35

.LBB0_1099:
	s_or_b64 exec, exec, s[64:65]
	s_mov_b32 s0, s37
	s_waitcnt lgkmcnt(0)
	s_barrier
	s_mov_b32 s1, s33
	v_mbcnt_lo_u32_b32 v0, -1, s0
	v_mbcnt_hi_u32_b32 v0, -1, v0
	v_lshl_or_b32 v0, s1, 6, v0
	v_readlane_b32 s0, v254, 0
	s_mov_b32 s4, s0
	s_mov_b32 s0, s37
	s_add_i32 s0, s0, 0x20120
	v_mov_b32_e32 v1, s0
	v_mov_b32_e32 v251, 0x20000
	ds_read_b64 v[206:207], v251 offset:288
	ds_read_b64 v[208:209], v251 offset:288
	ds_read_b64 v[210:211], v251 offset:288
	ds_read_b64 v[212:213], v251 offset:248
	ds_read_b64 v[214:215], v251 offset:288
	s_mov_b32 s0, 0
	s_add_i32 s0, s0, 0x20120
	v_readlane_b32 s1, v254, 1
	v_mov_b32_e32 v1, s0
	s_waitcnt lgkmcnt(0)
	v_readfirstlane_b32 s1, v207
	v_readfirstlane_b32 s2, v206
	s_mov_b32 s0, 0
	s_add_i32 s0, s0, 0x20120
	v_mov_b32_e32 v1, s0
	s_waitcnt lgkmcnt(0)
	v_readfirstlane_b32 s6, v209
	v_readfirstlane_b32 s7, v208
	s_mov_b32 s0, 0
	s_add_i32 s0, s0, 0x200f8
	v_mov_b32_e32 v1, s0
	s_waitcnt lgkmcnt(0)
	v_readfirstlane_b32 s10, v211
	v_readfirstlane_b32 s11, v210
	s_mov_b32 s0, s60
	s_mov_b32 s5, 0
	s_add_i32 s5, s5, 0x20120
	v_mov_b32_e32 v1, s5
	s_waitcnt lgkmcnt(0)
	v_readfirstlane_b32 s8, v213
	v_readfirstlane_b32 s9, v212
	v_and_b32_e32 v32, 63, v0
	v_ashrrev_i32_e32 v1, 6, v0
	v_mov_b32_e32 v106, 0
	v_cmp_gt_u32_e32 vcc, 8, v32
	s_waitcnt lgkmcnt(0)
	v_readfirstlane_b32 s12, v215
	v_readfirstlane_b32 s13, v214
	v_lshl_add_u32 v74, s4, 3, v1
	s_and_saveexec_b64 s[4:5], vcc
	s_cbranch_execz .LBB0_1101
	v_lshlrev_b32_e32 v1, 10, v32
	v_and_b32_e32 v1, 0x1800, v1
	v_add_u32_e32 v1, v74, v1
	v_and_b32_e32 v0, 1, v0
	s_add_u32 s14, s11, 0x1e78fd00
	v_lshl_or_b32 v0, v1, 1, v0
	s_addc_u32 s15, s10, 0
	v_ashrrev_i32_e32 v1, 31, v0
	v_lshl_add_u64 v[0:1], v[0:1], 2, s[14:15]
	flat_load_dword v106, v[0:1]

.LBB0_1145:
	s_or_b64 exec, exec, s[64:65]
	s_mov_b32 s0, s37
	s_waitcnt lgkmcnt(0)
	s_barrier
	s_mov_b32 s1, s33
	v_mbcnt_lo_u32_b32 v0, -1, s0
	v_mbcnt_hi_u32_b32 v0, -1, v0
	v_lshl_or_b32 v8, s1, 6, v0
	v_readlane_b32 s0, v254, 0
	s_mov_b32 s64, s0
	s_mov_b32 s0, s37
	s_add_i32 s0, s0, 0x20120
	v_mov_b32_e32 v0, s0
	v_mov_b32_e32 v251, 0x20000
	ds_read_b64 v[206:207], v251 offset:288
	ds_read_b64 v[208:209], v251 offset:288
	ds_read_b64 v[210:211], v251 offset:288
	ds_read_b64 v[212:213], v251 offset:288
	ds_read_b64 v[214:215], v251 offset:272
	ds_read_b64 v[216:217], v251 offset:40
	ds_read_b64 v[218:219], v251 offset:288
	ds_read_b64 v[224:225], v251 offset:288
	s_mov_b32 s0, 0
	s_add_i32 s0, s0, 0x20120
	v_readlane_b32 s1, v254, 1
	s_waitcnt lgkmcnt(0)
	v_readfirstlane_b32 s10, v206
	v_mov_b32_e32 v0, s0
	v_readfirstlane_b32 s1, v207
	s_mov_b32 s0, s60
	s_mov_b32 s2, 0
	s_add_i32 s2, s2, 0x20120
	s_waitcnt lgkmcnt(0)
	v_readfirstlane_b32 s17, v208
	v_mov_b32_e32 v0, s2
	v_readfirstlane_b32 s11, v209
	s_mov_b32 s2, 0
	s_add_i32 s2, s2, 0x20120
	v_readlane_b32 s4, v255, 13
	s_waitcnt lgkmcnt(0)
	v_readfirstlane_b32 s12, v210
	v_mov_b32_e32 v0, s2
	v_readfirstlane_b32 s13, v211
	v_readlane_b32 s5, v255, 14
	s_mov_b64 s[6:7], -1
	s_and_b64 vcc, exec, s[4:5]
	s_waitcnt lgkmcnt(0)
	v_readfirstlane_b32 s15, v213
	v_readfirstlane_b32 s14, v212
	s_cbranch_vccz .LBB0_1147
	s_mov_b32 s2, s37
	s_add_i32 s2, s2, 0x20110
	v_mov_b32_e32 v0, s2
	s_mov_b64 s[6:7], 0
	s_waitcnt lgkmcnt(0)
	v_readfirstlane_b32 s5, v215
	v_readfirstlane_b32 s4, v214
.LBB0_1147:
	s_andn2_b64 vcc, exec, s[6:7]
	s_cbranch_vccnz .LBB0_1149
	s_mov_b32 s2, s37
	s_add_i32 s2, s2, 0x20028
	v_mov_b32_e32 v0, s2
	s_waitcnt lgkmcnt(0)
	v_readfirstlane_b32 s4, v216
	v_readfirstlane_b32 s2, v217
	s_add_u32 s4, s4, 0x2000
	s_addc_u32 s5, s2, 0
.LBB0_1149:
	s_mov_b32 s2, s37
	s_add_i32 s2, s2, 0x20120
	v_mov_b32_e32 v0, s2
	s_mov_b32 s2, 0
	s_add_i32 s2, s2, 0x20120
	s_cmpk_lt_i32 s64, 0x100
	s_waitcnt lgkmcnt(0)
	v_readfirstlane_b32 s19, v218
	v_mov_b32_e32 v0, s2
	v_readfirstlane_b32 s18, v219
	v_readfirstlane_b32 s16, v8
	s_cselect_b64 s[6:7], -1, 0
	s_cmpk_gt_i32 s64, 0xff
	s_waitcnt lgkmcnt(0)
	v_readfirstlane_b32 s2, v225
	v_readfirstlane_b32 s20, v224
	s_cbranch_scc1 .LBB0_1155
	s_ashr_i32 s8, s64, 31
	s_lshr_b32 s8, s8, 29
	s_add_i32 s21, s64, s8
	s_and_b32 s8, s21, -8
	s_sub_i32 s22, s64, s8
	s_cmp_gt_i32 s22, -1
	s_mov_b64 s[8:9], -1
	s_cbranch_scc0 .LBB0_1152
	s_lshl_b32 s23, s22, 5
	s_mov_b64 s[8:9], 0

.LBB0_1234:
	s_mov_b32 s0, 0
	s_nop 0
	v_mbcnt_lo_u32_b32 v0, -1, s0
	v_mbcnt_hi_u32_b32 v0, -1, v0
	v_readlane_b32 s0, v254, 0
	v_lshl_or_b32 v0, s33, 6, v0
	s_mov_b32 s8, s0
	s_mov_b32 s0, 0
	s_add_i32 s0, s0, 0x20120
	v_mov_b32_e32 v1, s0
	v_readlane_b32 s1, v254, 1
	v_mov_b32_e32 v251, 0x20000
	ds_read_b64 v[206:207], v251 offset:288
	ds_read_b64 v[208:209], v251 offset:288
	ds_read_b64 v[210:211], v251 offset:272
	ds_read_b64 v[212:213], v251 offset:280
	s_mov_b32 s1, 0
	s_add_i32 s1, s1, 0x20120
	v_mov_b32_e32 v1, s1
	s_mov_b32 s1, 0
	s_waitcnt lgkmcnt(0)
	v_readfirstlane_b32 s2, v207
	v_readfirstlane_b32 s3, v206
	s_add_i32 s1, s1, 0x20110
	s_mov_b32 s0, 0
	v_mov_b32_e32 v1, s1
	s_add_i32 s0, s0, 0x20118
	v_mov_b32_e32 v1, s0
	s_ashr_i32 s9, s8, 31
	s_lshl_b64 s[8:9], s[8:9], 9
	v_ashrrev_i32_e32 v1, 31, v0
	v_lshl_add_u64 v[0:1], s[8:9], 0, v[0:1]
	s_mov_b64 s[8:9], 0x400000
	s_waitcnt lgkmcnt(0)
	v_readfirstlane_b32 s6, v209
	v_readfirstlane_b32 s7, v208
	v_readfirstlane_b32 s1, v211
	v_readfirstlane_b32 s0, v210
	v_readfirstlane_b32 s5, v213
	v_readfirstlane_b32 s4, v212
	v_cmp_gt_i64_e32 vcc, s[8:9], v[0:1]
	s_and_saveexec_b64 s[8:9], vcc
	s_cbranch_execz .LBB0_1237
	s_add_u32 s8, s3, 0x3600
	s_addc_u32 s9, s2, 0
	s_add_u32 s2, s7, 0x57327d00
	s_addc_u32 s3, s6, 0
	s_add_u32 s2, s2, 0x10000
	v_lshlrev_b64 v[4:5], 4, v[0:1]
	s_addc_u32 s3, s3, 0
	v_lshlrev_b32_e32 v8, 2, v0
	v_lshl_add_u64 v[2:3], s[4:5], 0, v[4:5]
	v_lshl_add_u64 v[4:5], s[8:9], 0, v[4:5]
	s_mov_b64 s[4:5], 0
	v_mov_b32_e32 v7, 0
	v_mov_b32_e32 v9, 0x358637bd
	s_mov_b64 s[6:7], 0x20000
	s_mov_b64 s[8:9], 0x200000
	s_mov_b64 s[10:11], 0x3dffff
